# GEMM K-loops (G1/G2/G3): keep the B half-0 fragments in 16 spare VGPRs instead of re-reading them from LDS in sub-phases 4 and 8
# speedup vs baseline: 1.0034x; 1.0034x over previous
.LBB0_247:
	s_add_u32 s50, s48, 0x80
	s_addc_u32 s51, s49, 0
	s_add_i32 s74, 0, 0x10000
	v_add_u32_e32 v220, s74, v147
	v_add_u32_e32 v221, s74, v148
	ds_read_b128 v[222:225], v220
	ds_read_b128 v[230:233], v220 offset:2048
	ds_read_b128 v[226:229], v221
	ds_read_b128 v[234:237], v221 offset:2048
	s_cmp_eq_u32 s73, 12
	s_cselect_b32 s53, s5, s51
	s_cselect_b32 s52, s43, s50
	s_cselect_b32 s51, s8, s72
	s_cselect_b32 s50, s9, s67
	s_add_i32 s75, s31, s55
	v_lshl_add_u64 v[142:143], s[48:49], 0, v[140:141]
	s_mov_b32 m0, s75
	ds_read_b128 v[168:171], v150
	ds_read_b128 v[182:185], v150 offset:2048
	ds_read_b128 v[172:175], v151
	ds_read_b128 v[186:189], v151 offset:2048
	ds_read_b128 v[190:193], v150 offset:4096
	ds_read_b128 v[198:201], v150 offset:6144
	ds_read_b128 v[194:197], v151 offset:4096
	ds_read_b128 v[202:205], v151 offset:6144
	global_load_lds_dwordx4 v[142:143], off
	v_lshl_add_u64 v[142:143], s[48:49], 0, v[138:139]
	s_add_i32 m0, s75, 0x2000
	s_nop 0
	global_load_lds_dwordx4 v[142:143], off
	s_waitcnt vmcnt(6)
	s_waitcnt lgkmcnt(0)
	s_barrier
	s_setprio 1
	s_waitcnt lgkmcnt(0)
	v_mfma_scale_f32_16x16x128_f8f6f4 v[128:131], v[222:229], v[168:175], v[128:131], v1, v1 op_sel_hi:[0,0,0]
	v_mfma_scale_f32_16x16x128_f8f6f4 v[124:127], v[230:237], v[168:175], v[124:127], v1, v1 op_sel_hi:[0,0,0]
	v_mfma_scale_f32_16x16x128_f8f6f4 v[120:123], v[222:229], v[182:189], v[120:123], v1, v1 op_sel_hi:[0,0,0]
	v_mfma_scale_f32_16x16x128_f8f6f4 v[112:115], v[230:237], v[182:189], v[112:115], v1, v1 op_sel_hi:[0,0,0]
	v_mfma_scale_f32_16x16x128_f8f6f4 v[104:107], v[222:229], v[190:197], v[104:107], v1, v1 op_sel_hi:[0,0,0]
	v_mfma_scale_f32_16x16x128_f8f6f4 v[96:99], v[230:237], v[190:197], v[96:99], v1, v1 op_sel_hi:[0,0,0]
	v_mfma_scale_f32_16x16x128_f8f6f4 v[88:91], v[222:229], v[198:205], v[88:91], v1, v1 op_sel_hi:[0,0,0]
	v_mfma_scale_f32_16x16x128_f8f6f4 v[80:83], v[230:237], v[198:205], v[80:83], v1, v1 op_sel_hi:[0,0,0]
	s_setprio 0
	s_barrier
	s_add_i32 s75, 0, 0x14000
	v_add_u32_e32 v142, s75, v147
	v_add_u32_e32 v143, s75, v148
	s_mov_b32 m0, s56
	ds_read_b128 v[152:155], v142
	ds_read_b128 v[160:163], v142 offset:2048
	ds_read_b128 v[156:159], v143
	ds_read_b128 v[164:167], v143 offset:2048
	v_lshl_add_u64 v[142:143], s[50:51], 0, v[2:3]
	global_load_lds_dwordx4 v[142:143], off
	v_lshl_add_u64 v[144:145], s[50:51], 0, v[134:135]
	s_mov_b32 m0, s57
	s_nop 0
	global_load_lds_dwordx4 v[144:145], off
	s_waitcnt vmcnt(6)
	s_waitcnt lgkmcnt(0)
	s_barrier
	s_setprio 1
	s_waitcnt lgkmcnt(0)
	v_mfma_scale_f32_16x16x128_f8f6f4 v[116:119], v[152:159], v[168:175], v[116:119], v1, v1 op_sel_hi:[0,0,0]
	v_mfma_scale_f32_16x16x128_f8f6f4 v[108:111], v[160:167], v[168:175], v[108:111], v1, v1 op_sel_hi:[0,0,0]
	v_mfma_scale_f32_16x16x128_f8f6f4 v[100:103], v[152:159], v[182:189], v[100:103], v1, v1 op_sel_hi:[0,0,0]
	v_mfma_scale_f32_16x16x128_f8f6f4 v[92:95], v[160:167], v[182:189], v[92:95], v1, v1 op_sel_hi:[0,0,0]
	v_mfma_scale_f32_16x16x128_f8f6f4 v[84:87], v[152:159], v[190:197], v[84:87], v1, v1 op_sel_hi:[0,0,0]
	v_mfma_scale_f32_16x16x128_f8f6f4 v[76:79], v[160:167], v[190:197], v[76:79], v1, v1 op_sel_hi:[0,0,0]
	v_mfma_scale_f32_16x16x128_f8f6f4 v[72:75], v[152:159], v[198:205], v[72:75], v1, v1 op_sel_hi:[0,0,0]
	v_mfma_scale_f32_16x16x128_f8f6f4 v[68:71], v[160:167], v[198:205], v[68:71], v1, v1 op_sel_hi:[0,0,0]
	s_setprio 0
	s_barrier
	s_add_u32 s80, s52, 0x40000
	s_addc_u32 s81, s53, 0
	s_add_i32 s75, s75, s55
	v_lshl_add_u64 v[176:177], s[80:81], 0, v[136:137]
	s_mov_b32 m0, s75
	ds_read_b128 v[168:171], v150 offset:16384
	ds_read_b128 v[182:185], v150 offset:18432
	ds_read_b128 v[172:175], v151 offset:16384
	ds_read_b128 v[186:189], v151 offset:18432
	ds_read_b128 v[190:193], v150 offset:20480
	ds_read_b128 v[198:201], v150 offset:22528
	ds_read_b128 v[194:197], v151 offset:20480
	ds_read_b128 v[202:205], v151 offset:22528
	global_load_lds_dwordx4 v[176:177], off
	v_lshl_add_u64 v[176:177], s[80:81], 0, v[132:133]
	s_add_i32 m0, s75, 0x2000
	s_nop 0
	global_load_lds_dwordx4 v[176:177], off
	s_waitcnt vmcnt(6)
	s_waitcnt lgkmcnt(0)
	s_barrier
	s_setprio 1
	s_waitcnt lgkmcnt(0)
	v_mfma_scale_f32_16x16x128_f8f6f4 v[52:55], v[152:159], v[168:175], v[52:55], v1, v1 op_sel_hi:[0,0,0]
	v_mfma_scale_f32_16x16x128_f8f6f4 v[44:47], v[160:167], v[168:175], v[44:47], v1, v1 op_sel_hi:[0,0,0]
	v_mfma_scale_f32_16x16x128_f8f6f4 v[36:39], v[152:159], v[182:189], v[36:39], v1, v1 op_sel_hi:[0,0,0]
	v_mfma_scale_f32_16x16x128_f8f6f4 v[28:31], v[160:167], v[182:189], v[28:31], v1, v1 op_sel_hi:[0,0,0]
	v_mfma_scale_f32_16x16x128_f8f6f4 v[20:23], v[152:159], v[190:197], v[20:23], v1, v1 op_sel_hi:[0,0,0]
	v_mfma_scale_f32_16x16x128_f8f6f4 v[12:15], v[160:167], v[190:197], v[12:15], v1, v1 op_sel_hi:[0,0,0]
	v_mfma_scale_f32_16x16x128_f8f6f4 v[8:11], v[152:159], v[198:205], v[8:11], v1, v1 op_sel_hi:[0,0,0]
	v_mfma_scale_f32_16x16x128_f8f6f4 v[4:7], v[160:167], v[198:205], v[4:7], v1, v1 op_sel_hi:[0,0,0]
	s_setprio 0
	s_barrier
	s_add_u32 s80, s50, 0x40000
	s_addc_u32 s81, s51, 0
	s_mov_b32 m0, s58
	v_lshl_add_u64 v[176:177], s[80:81], 0, v[2:3]
	global_load_lds_dwordx4 v[176:177], off
	v_lshl_add_u64 v[176:177], s[80:81], 0, v[134:135]
	s_mov_b32 m0, s59
	s_nop 0
	global_load_lds_dwordx4 v[176:177], off
	s_waitcnt vmcnt(6)
	s_waitcnt lgkmcnt(0)
	s_barrier
	s_setprio 1
	s_waitcnt lgkmcnt(0)
	v_mfma_scale_f32_16x16x128_f8f6f4 v[64:67], v[222:229], v[168:175], v[64:67], v1, v1 op_sel_hi:[0,0,0]
	v_mfma_scale_f32_16x16x128_f8f6f4 v[60:63], v[230:237], v[168:175], v[60:63], v1, v1 op_sel_hi:[0,0,0]
	v_mfma_scale_f32_16x16x128_f8f6f4 v[56:59], v[222:229], v[182:189], v[56:59], v1, v1 op_sel_hi:[0,0,0]
	v_mfma_scale_f32_16x16x128_f8f6f4 v[48:51], v[230:237], v[182:189], v[48:51], v1, v1 op_sel_hi:[0,0,0]
	v_mfma_scale_f32_16x16x128_f8f6f4 v[40:43], v[222:229], v[190:197], v[40:43], v1, v1 op_sel_hi:[0,0,0]
	v_mfma_scale_f32_16x16x128_f8f6f4 v[32:35], v[230:237], v[190:197], v[32:35], v1, v1 op_sel_hi:[0,0,0]
	v_mfma_scale_f32_16x16x128_f8f6f4 v[24:27], v[222:229], v[198:205], v[24:27], v1, v1 op_sel_hi:[0,0,0]
	v_mfma_scale_f32_16x16x128_f8f6f4 v[16:19], v[230:237], v[198:205], v[16:19], v1, v1 op_sel_hi:[0,0,0]
	s_setprio 0
	s_barrier
	v_add_u32_e32 v220, s31, v147
	v_add_u32_e32 v221, s31, v148
	ds_read_b128 v[222:225], v220
	ds_read_b128 v[230:233], v220 offset:2048
	ds_read_b128 v[226:229], v221
	ds_read_b128 v[234:237], v221 offset:2048
	s_add_i32 s74, s74, s55
	v_lshl_add_u64 v[176:177], s[52:53], 0, v[136:137]
	s_mov_b32 m0, s74
	ds_read_b128 v[168:171], v150 offset:32768
	ds_read_b128 v[182:185], v150 offset:34816
	ds_read_b128 v[172:175], v151 offset:32768
	ds_read_b128 v[186:189], v151 offset:34816
	ds_read_b128 v[190:193], v150 offset:36864
	ds_read_b128 v[198:201], v150 offset:38912
	ds_read_b128 v[194:197], v151 offset:36864
	ds_read_b128 v[202:205], v151 offset:38912
	global_load_lds_dwordx4 v[176:177], off
	v_lshl_add_u64 v[176:177], s[52:53], 0, v[132:133]
	s_add_i32 m0, s74, 0x2000
	s_nop 0
	global_load_lds_dwordx4 v[176:177], off
	s_waitcnt vmcnt(6)
	s_waitcnt lgkmcnt(0)
	s_barrier
	s_setprio 1
	s_waitcnt lgkmcnt(0)
	v_mfma_scale_f32_16x16x128_f8f6f4 v[128:131], v[222:229], v[168:175], v[128:131], v1, v1 op_sel_hi:[0,0,0]
	v_mfma_scale_f32_16x16x128_f8f6f4 v[124:127], v[230:237], v[168:175], v[124:127], v1, v1 op_sel_hi:[0,0,0]
	v_mfma_scale_f32_16x16x128_f8f6f4 v[120:123], v[222:229], v[182:189], v[120:123], v1, v1 op_sel_hi:[0,0,0]
	v_mfma_scale_f32_16x16x128_f8f6f4 v[112:115], v[230:237], v[182:189], v[112:115], v1, v1 op_sel_hi:[0,0,0]
	v_mfma_scale_f32_16x16x128_f8f6f4 v[104:107], v[222:229], v[190:197], v[104:107], v1, v1 op_sel_hi:[0,0,0]
	v_mfma_scale_f32_16x16x128_f8f6f4 v[96:99], v[230:237], v[190:197], v[96:99], v1, v1 op_sel_hi:[0,0,0]
	v_mfma_scale_f32_16x16x128_f8f6f4 v[88:91], v[222:229], v[198:205], v[88:91], v1, v1 op_sel_hi:[0,0,0]
	v_mfma_scale_f32_16x16x128_f8f6f4 v[80:83], v[230:237], v[198:205], v[80:83], v1, v1 op_sel_hi:[0,0,0]
	s_setprio 0
	s_barrier
	s_add_i32 s74, 0, 0x1c000
	s_mov_b32 m0, s60
	v_add_u32_e32 v156, s74, v147
	v_add_u32_e32 v164, s74, v148
	v_lshl_add_u64 v[142:143], v[142:143], 0, s[20:21]
	ds_read_b128 v[152:155], v156
	ds_read_b128 v[160:163], v156 offset:2048
	ds_read_b128 v[156:159], v164
	ds_read_b128 v[164:167], v164 offset:2048
	global_load_lds_dwordx4 v[142:143], off
	v_lshl_add_u64 v[142:143], v[144:145], 0, s[20:21]
	s_mov_b32 m0, s61
	s_nop 0
	global_load_lds_dwordx4 v[142:143], off
	s_waitcnt vmcnt(6)
	s_waitcnt lgkmcnt(0)
	s_barrier
	s_setprio 1
	s_waitcnt lgkmcnt(0)
	v_mfma_scale_f32_16x16x128_f8f6f4 v[116:119], v[152:159], v[168:175], v[116:119], v1, v1 op_sel_hi:[0,0,0]
	v_mfma_scale_f32_16x16x128_f8f6f4 v[108:111], v[160:167], v[168:175], v[108:111], v1, v1 op_sel_hi:[0,0,0]
	v_mfma_scale_f32_16x16x128_f8f6f4 v[100:103], v[152:159], v[182:189], v[100:103], v1, v1 op_sel_hi:[0,0,0]
	v_mfma_scale_f32_16x16x128_f8f6f4 v[92:95], v[160:167], v[182:189], v[92:95], v1, v1 op_sel_hi:[0,0,0]
	v_mfma_scale_f32_16x16x128_f8f6f4 v[84:87], v[152:159], v[190:197], v[84:87], v1, v1 op_sel_hi:[0,0,0]
	v_mfma_scale_f32_16x16x128_f8f6f4 v[76:79], v[160:167], v[190:197], v[76:79], v1, v1 op_sel_hi:[0,0,0]
	v_mfma_scale_f32_16x16x128_f8f6f4 v[72:75], v[152:159], v[198:205], v[72:75], v1, v1 op_sel_hi:[0,0,0]
	v_mfma_scale_f32_16x16x128_f8f6f4 v[68:71], v[160:167], v[198:205], v[68:71], v1, v1 op_sel_hi:[0,0,0]
	s_setprio 0
	s_barrier
	s_add_u32 s52, s52, 0x40080
	s_addc_u32 s53, s53, 0
	s_add_i32 s74, s74, s55
	v_lshl_add_u64 v[142:143], s[52:53], 0, v[136:137]
	s_mov_b32 m0, s74
	ds_read_b128 v[168:171], v150 offset:49152
	ds_read_b128 v[182:185], v150 offset:51200
	ds_read_b128 v[172:175], v151 offset:49152
	ds_read_b128 v[186:189], v151 offset:51200
	ds_read_b128 v[190:193], v150 offset:53248
	ds_read_b128 v[198:201], v150 offset:55296
	ds_read_b128 v[194:197], v151 offset:53248
	ds_read_b128 v[202:205], v151 offset:55296
	global_load_lds_dwordx4 v[142:143], off
	v_lshl_add_u64 v[142:143], s[52:53], 0, v[132:133]
	s_add_i32 m0, s74, 0x2000
	s_nop 0
	global_load_lds_dwordx4 v[142:143], off
	s_waitcnt vmcnt(6)
	s_waitcnt lgkmcnt(0)
	s_barrier
	s_setprio 1
	s_waitcnt lgkmcnt(0)
	v_mfma_scale_f32_16x16x128_f8f6f4 v[52:55], v[152:159], v[168:175], v[52:55], v1, v1 op_sel_hi:[0,0,0]
	v_mfma_scale_f32_16x16x128_f8f6f4 v[44:47], v[160:167], v[168:175], v[44:47], v1, v1 op_sel_hi:[0,0,0]
	v_mfma_scale_f32_16x16x128_f8f6f4 v[36:39], v[152:159], v[182:189], v[36:39], v1, v1 op_sel_hi:[0,0,0]
	v_mfma_scale_f32_16x16x128_f8f6f4 v[28:31], v[160:167], v[182:189], v[28:31], v1, v1 op_sel_hi:[0,0,0]
	v_mfma_scale_f32_16x16x128_f8f6f4 v[20:23], v[152:159], v[190:197], v[20:23], v1, v1 op_sel_hi:[0,0,0]
	v_mfma_scale_f32_16x16x128_f8f6f4 v[12:15], v[160:167], v[190:197], v[12:15], v1, v1 op_sel_hi:[0,0,0]
	v_mfma_scale_f32_16x16x128_f8f6f4 v[8:11], v[152:159], v[198:205], v[8:11], v1, v1 op_sel_hi:[0,0,0]
	v_mfma_scale_f32_16x16x128_f8f6f4 v[4:7], v[160:167], v[198:205], v[4:7], v1, v1 op_sel_hi:[0,0,0]
	s_setprio 0
	s_barrier
	s_add_u32 s50, s50, 0x40080
	s_addc_u32 s51, s51, 0
	s_mov_b32 m0, s62
	v_lshl_add_u64 v[142:143], s[50:51], 0, v[2:3]
	global_load_lds_dwordx4 v[142:143], off
	v_lshl_add_u64 v[142:143], s[50:51], 0, v[134:135]
	s_mov_b32 m0, s63
	s_nop 0
	global_load_lds_dwordx4 v[142:143], off
	s_waitcnt vmcnt(6)
	s_waitcnt lgkmcnt(0)
	s_barrier
	s_setprio 1
	s_waitcnt lgkmcnt(0)
	v_mfma_scale_f32_16x16x128_f8f6f4 v[64:67], v[222:229], v[168:175], v[64:67], v1, v1 op_sel_hi:[0,0,0]
	v_mfma_scale_f32_16x16x128_f8f6f4 v[60:63], v[230:237], v[168:175], v[60:63], v1, v1 op_sel_hi:[0,0,0]
	v_mfma_scale_f32_16x16x128_f8f6f4 v[56:59], v[222:229], v[182:189], v[56:59], v1, v1 op_sel_hi:[0,0,0]
	v_mfma_scale_f32_16x16x128_f8f6f4 v[48:51], v[230:237], v[182:189], v[48:51], v1, v1 op_sel_hi:[0,0,0]
	v_mfma_scale_f32_16x16x128_f8f6f4 v[40:43], v[222:229], v[190:197], v[40:43], v1, v1 op_sel_hi:[0,0,0]
	v_mfma_scale_f32_16x16x128_f8f6f4 v[32:35], v[230:237], v[190:197], v[32:35], v1, v1 op_sel_hi:[0,0,0]
	v_mfma_scale_f32_16x16x128_f8f6f4 v[24:27], v[222:229], v[198:205], v[24:27], v1, v1 op_sel_hi:[0,0,0]
	v_mfma_scale_f32_16x16x128_f8f6f4 v[16:19], v[230:237], v[198:205], v[16:19], v1, v1 op_sel_hi:[0,0,0]
	s_setprio 0
	s_barrier
	s_add_i32 s73, s73, 2
	s_add_u32 s67, s67, 0x100
	s_addc_u32 s72, s72, 0
	s_add_u32 s48, s48, 0x100
	s_addc_u32 s49, s49, 0
	s_cmp_gt_u32 s73, 13
	s_cbranch_scc0 .LBB0_247
	v_lshl_or_b32 v144, s65, 8, v149
	v_lshl_add_u32 v156, s66, 8, v146
	v_ashrrev_i32_e32 v145, 31, v144
	v_mov_b64_e32 v[142:143], s[0:1]
	v_mad_i64_i32 v[152:153], s[8:9], v156, s94, v[142:143]
	v_lshlrev_b64 v[144:145], 1, v[144:145]
	v_pk_mul_f32 v[130:131], v[130:131], s[22:23] op_sel_hi:[1,0]
	v_pk_mul_f32 v[128:129], v[128:129], s[22:23] op_sel_hi:[1,0]
	v_pk_mul_f32 v[154:155], v[126:127], s[22:23] op_sel_hi:[1,0]
	v_pk_mul_f32 v[126:127], v[124:125], s[22:23] op_sel_hi:[1,0]
	v_lshl_add_u64 v[152:153], v[152:153], 0, v[144:145]
	v_cvt_pk_bf16_f32 v124, v128, v129
	v_cvt_pk_bf16_f32 v125, v130, v131
	v_cvt_pk_bf16_f32 v126, v126, v127
	v_cvt_pk_bf16_f32 v127, v154, v155
	global_store_dwordx4 v[152:153], v[124:127], off
	v_pk_mul_f32 v[118:119], v[118:119], s[22:23] op_sel_hi:[1,0]
	v_pk_mul_f32 v[116:117], v[116:117], s[22:23] op_sel_hi:[1,0]
	v_pk_mul_f32 v[124:125], v[110:111], s[22:23] op_sel_hi:[1,0]
	v_pk_mul_f32 v[110:111], v[108:109], s[22:23] op_sel_hi:[1,0]
	v_cvt_pk_bf16_f32 v108, v116, v117
	v_cvt_pk_bf16_f32 v109, v118, v119
	v_cvt_pk_bf16_f32 v110, v110, v111
	v_cvt_pk_bf16_f32 v111, v124, v125
	global_store_dwordx4 v[152:153], v[108:111], off offset:256
	v_pk_mul_f32 v[114:115], v[114:115], s[22:23] op_sel_hi:[1,0]
	v_pk_mul_f32 v[112:113], v[112:113], s[22:23] op_sel_hi:[1,0]
	v_or_b32_e32 v108, 16, v156
	v_mad_i64_i32 v[108:109], s[8:9], v108, s94, v[142:143]
	v_lshl_add_u64 v[116:117], v[108:109], 0, v[144:145]
	v_pk_mul_f32 v[110:111], v[122:123], s[22:23] op_sel_hi:[1,0]
	v_pk_mul_f32 v[108:109], v[120:121], s[22:23] op_sel_hi:[1,0]
	v_pk_mul_f32 v[102:103], v[102:103], s[22:23] op_sel_hi:[1,0]
	v_cvt_pk_bf16_f32 v108, v108, v109
	v_cvt_pk_bf16_f32 v109, v110, v111
	v_cvt_pk_bf16_f32 v110, v112, v113
	v_cvt_pk_bf16_f32 v111, v114, v115
	global_store_dwordx4 v[116:117], v[108:111], off
	v_pk_mul_f32 v[100:101], v[100:101], s[22:23] op_sel_hi:[1,0]
	v_pk_mul_f32 v[98:99], v[98:99], s[22:23] op_sel_hi:[1,0]
	v_pk_mul_f32 v[108:109], v[94:95], s[22:23] op_sel_hi:[1,0]
	v_pk_mul_f32 v[94:95], v[92:93], s[22:23] op_sel_hi:[1,0]
	v_cvt_pk_bf16_f32 v92, v100, v101
	v_cvt_pk_bf16_f32 v93, v102, v103
	v_cvt_pk_bf16_f32 v94, v94, v95
	v_cvt_pk_bf16_f32 v95, v108, v109
	global_store_dwordx4 v[116:117], v[92:95], off offset:256
	v_pk_mul_f32 v[96:97], v[96:97], s[22:23] op_sel_hi:[1,0]
	v_pk_mul_f32 v[86:87], v[86:87], s[22:23] op_sel_hi:[1,0]
	v_or_b32_e32 v92, 32, v156
	v_mad_i64_i32 v[92:93], s[8:9], v92, s94, v[142:143]
	v_lshl_add_u64 v[100:101], v[92:93], 0, v[144:145]
	v_pk_mul_f32 v[94:95], v[106:107], s[22:23] op_sel_hi:[1,0]
	v_pk_mul_f32 v[92:93], v[104:105], s[22:23] op_sel_hi:[1,0]
	v_pk_mul_f32 v[84:85], v[84:85], s[22:23] op_sel_hi:[1,0]
	v_cvt_pk_bf16_f32 v92, v92, v93
	v_cvt_pk_bf16_f32 v93, v94, v95
	v_cvt_pk_bf16_f32 v94, v96, v97
	v_cvt_pk_bf16_f32 v95, v98, v99
	global_store_dwordx4 v[100:101], v[92:95], off
	v_pk_mul_f32 v[82:83], v[82:83], s[22:23] op_sel_hi:[1,0]
	v_pk_mul_f32 v[80:81], v[80:81], s[22:23] op_sel_hi:[1,0]
	v_pk_mul_f32 v[92:93], v[78:79], s[22:23] op_sel_hi:[1,0]
	v_pk_mul_f32 v[78:79], v[76:77], s[22:23] op_sel_hi:[1,0]
	v_cvt_pk_bf16_f32 v76, v84, v85
	v_cvt_pk_bf16_f32 v77, v86, v87
	v_cvt_pk_bf16_f32 v78, v78, v79
	v_cvt_pk_bf16_f32 v79, v92, v93
	global_store_dwordx4 v[100:101], v[76:79], off offset:256
	v_pk_mul_f32 v[74:75], v[74:75], s[22:23] op_sel_hi:[1,0]
	v_pk_mul_f32 v[72:73], v[72:73], s[22:23] op_sel_hi:[1,0]
	v_or_b32_e32 v76, 48, v156
	v_mad_i64_i32 v[76:77], s[8:9], v76, s94, v[142:143]
	v_lshl_add_u64 v[84:85], v[76:77], 0, v[144:145]
	v_pk_mul_f32 v[78:79], v[90:91], s[22:23] op_sel_hi:[1,0]
	v_pk_mul_f32 v[76:77], v[88:89], s[22:23] op_sel_hi:[1,0]
	v_pk_mul_f32 v[66:67], v[66:67], s[22:23] op_sel_hi:[1,0]
	v_cvt_pk_bf16_f32 v76, v76, v77
	v_cvt_pk_bf16_f32 v77, v78, v79
	v_cvt_pk_bf16_f32 v78, v80, v81
	v_cvt_pk_bf16_f32 v79, v82, v83
	global_store_dwordx4 v[84:85], v[76:79], off
	v_pk_mul_f32 v[64:65], v[64:65], s[22:23] op_sel_hi:[1,0]
	v_pk_mul_f32 v[54:55], v[54:55], s[22:23] op_sel_hi:[1,0]
	v_pk_mul_f32 v[76:77], v[70:71], s[22:23] op_sel_hi:[1,0]
	v_pk_mul_f32 v[70:71], v[68:69], s[22:23] op_sel_hi:[1,0]
	v_cvt_pk_bf16_f32 v68, v72, v73
	v_cvt_pk_bf16_f32 v69, v74, v75
	v_cvt_pk_bf16_f32 v70, v70, v71
	v_cvt_pk_bf16_f32 v71, v76, v77
	global_store_dwordx4 v[84:85], v[68:71], off offset:256
	v_pk_mul_f32 v[52:53], v[52:53], s[22:23] op_sel_hi:[1,0]
	v_pk_mul_f32 v[50:51], v[50:51], s[22:23] op_sel_hi:[1,0]
	v_add_u32_e32 v68, 0x80, v156
	v_mad_i64_i32 v[68:69], s[8:9], v68, s94, v[142:143]
	v_pk_mul_f32 v[70:71], v[62:63], s[22:23] op_sel_hi:[1,0]
	v_pk_mul_f32 v[62:63], v[60:61], s[22:23] op_sel_hi:[1,0]
	v_lshl_add_u64 v[68:69], v[68:69], 0, v[144:145]
	v_cvt_pk_bf16_f32 v60, v64, v65
	v_cvt_pk_bf16_f32 v61, v66, v67
	v_cvt_pk_bf16_f32 v62, v62, v63
	v_cvt_pk_bf16_f32 v63, v70, v71
	global_store_dwordx4 v[68:69], v[60:63], off
	v_pk_mul_f32 v[48:49], v[48:49], s[22:23] op_sel_hi:[1,0]
	v_pk_mul_f32 v[38:39], v[38:39], s[22:23] op_sel_hi:[1,0]
	v_pk_mul_f32 v[60:61], v[46:47], s[22:23] op_sel_hi:[1,0]
	v_pk_mul_f32 v[46:47], v[44:45], s[22:23] op_sel_hi:[1,0]
	v_cvt_pk_bf16_f32 v44, v52, v53
	v_cvt_pk_bf16_f32 v45, v54, v55
	v_cvt_pk_bf16_f32 v46, v46, v47
	v_cvt_pk_bf16_f32 v47, v60, v61
	global_store_dwordx4 v[68:69], v[44:47], off offset:256
	v_pk_mul_f32 v[36:37], v[36:37], s[22:23] op_sel_hi:[1,0]
	v_pk_mul_f32 v[34:35], v[34:35], s[22:23] op_sel_hi:[1,0]
	v_add_u32_e32 v44, 0x90, v156
	v_mad_i64_i32 v[44:45], s[8:9], v44, s94, v[142:143]
	v_lshl_add_u64 v[52:53], v[44:45], 0, v[144:145]
	v_pk_mul_f32 v[46:47], v[58:59], s[22:23] op_sel_hi:[1,0]
	v_pk_mul_f32 v[44:45], v[56:57], s[22:23] op_sel_hi:[1,0]
	v_pk_mul_f32 v[32:33], v[32:33], s[22:23] op_sel_hi:[1,0]
	v_cvt_pk_bf16_f32 v44, v44, v45
	v_cvt_pk_bf16_f32 v45, v46, v47
	v_cvt_pk_bf16_f32 v46, v48, v49
	v_cvt_pk_bf16_f32 v47, v50, v51
	global_store_dwordx4 v[52:53], v[44:47], off
	v_pk_mul_f32 v[22:23], v[22:23], s[22:23] op_sel_hi:[1,0]
	v_pk_mul_f32 v[20:21], v[20:21], s[22:23] op_sel_hi:[1,0]
	v_pk_mul_f32 v[44:45], v[30:31], s[22:23] op_sel_hi:[1,0]
	v_pk_mul_f32 v[30:31], v[28:29], s[22:23] op_sel_hi:[1,0]
	v_cvt_pk_bf16_f32 v28, v36, v37
	v_cvt_pk_bf16_f32 v29, v38, v39
	v_cvt_pk_bf16_f32 v30, v30, v31
	v_cvt_pk_bf16_f32 v31, v44, v45
	global_store_dwordx4 v[52:53], v[28:31], off offset:256
	v_pk_mul_f32 v[18:19], v[18:19], s[22:23] op_sel_hi:[1,0]
	v_pk_mul_f32 v[16:17], v[16:17], s[22:23] op_sel_hi:[1,0]
	v_add_u32_e32 v28, 0xa0, v156
	v_mad_i64_i32 v[28:29], s[8:9], v28, s94, v[142:143]
	v_lshl_add_u64 v[36:37], v[28:29], 0, v[144:145]
	v_pk_mul_f32 v[30:31], v[42:43], s[22:23] op_sel_hi:[1,0]
	v_pk_mul_f32 v[28:29], v[40:41], s[22:23] op_sel_hi:[1,0]
	v_pk_mul_f32 v[10:11], v[10:11], s[22:23] op_sel_hi:[1,0]
	v_cvt_pk_bf16_f32 v28, v28, v29
	v_cvt_pk_bf16_f32 v29, v30, v31
	v_cvt_pk_bf16_f32 v30, v32, v33
	v_cvt_pk_bf16_f32 v31, v34, v35
	global_store_dwordx4 v[36:37], v[28:31], off
	v_pk_mul_f32 v[8:9], v[8:9], s[22:23] op_sel_hi:[1,0]
	s_and_b64 vcc, exec, s[40:41]
	v_pk_mul_f32 v[28:29], v[14:15], s[22:23] op_sel_hi:[1,0]
	v_pk_mul_f32 v[14:15], v[12:13], s[22:23] op_sel_hi:[1,0]
	v_cvt_pk_bf16_f32 v12, v20, v21
	v_cvt_pk_bf16_f32 v13, v22, v23
	v_cvt_pk_bf16_f32 v14, v14, v15
	v_cvt_pk_bf16_f32 v15, v28, v29
	global_store_dwordx4 v[36:37], v[12:15], off offset:256
	s_mov_b32 s65, s4
	s_mov_b32 s66, s42
	v_add_u32_e32 v12, 0xb0, v156
	v_mad_i64_i32 v[12:13], s[8:9], v12, s94, v[142:143]
	v_lshl_add_u64 v[20:21], v[12:13], 0, v[144:145]
	v_pk_mul_f32 v[14:15], v[26:27], s[22:23] op_sel_hi:[1,0]
	v_pk_mul_f32 v[12:13], v[24:25], s[22:23] op_sel_hi:[1,0]
	s_mov_b64 s[48:49], s[46:47]
	v_cvt_pk_bf16_f32 v12, v12, v13
	v_cvt_pk_bf16_f32 v13, v14, v15
	v_cvt_pk_bf16_f32 v14, v16, v17
	v_cvt_pk_bf16_f32 v15, v18, v19
	global_store_dwordx4 v[20:21], v[12:15], off
	s_mov_b64 s[50:51], s[44:45]
	s_nop 0
	v_pk_mul_f32 v[12:13], v[6:7], s[22:23] op_sel_hi:[1,0]
	v_pk_mul_f32 v[6:7], v[4:5], s[22:23] op_sel_hi:[1,0]
	v_cvt_pk_bf16_f32 v4, v8, v9
	v_cvt_pk_bf16_f32 v5, v10, v11
	v_cvt_pk_bf16_f32 v6, v6, v7
	v_cvt_pk_bf16_f32 v7, v12, v13
	global_store_dwordx4 v[20:21], v[4:7], off offset:256
	s_cbranch_vccz .LBB0_240
	s_waitcnt vmcnt(0)
	v_readlane_b32 s64, v253, 27
	v_readlane_b32 s66, v253, 29
	s_cmpk_gt_u32 s6, 0xff
	v_readlane_b32 s65, v253, 28
	v_readlane_b32 s67, v253, 30
	s_cbranch_scc1 .LBB0_251
	s_barrier

.LBB0_430:
	s_add_u32 s56, s54, 0x80
	s_addc_u32 s57, s55, 0
	s_add_i32 vcc_lo, 0, 0x10000
	v_add_u32_e32 v220, vcc_lo, v143
	v_add_u32_e32 v221, vcc_lo, v144
	ds_read_b128 v[222:225], v220
	ds_read_b128 v[230:233], v220 offset:2048
	ds_read_b128 v[226:229], v221
	ds_read_b128 v[234:237], v221 offset:2048
	s_cmp_eq_u32 s97, 12
	s_cselect_b32 s59, s5, s57
	s_cselect_b32 s58, s43, s56
	s_cselect_b32 s57, s8, s96
	s_cselect_b32 s56, s9, s89
	s_add_i32 s76, s31, s64
	v_lshl_add_u64 v[172:173], s[54:55], 0, v[140:141]
	s_mov_b32 m0, s76
	ds_read_b128 v[164:167], v146
	ds_read_b128 v[182:185], v146 offset:2048
	ds_read_b128 v[168:171], v147
	ds_read_b128 v[186:189], v147 offset:2048
	ds_read_b128 v[190:193], v146 offset:4096
	ds_read_b128 v[198:201], v146 offset:6144
	ds_read_b128 v[194:197], v147 offset:4096
	ds_read_b128 v[202:205], v147 offset:6144
	global_load_lds_dwordx4 v[172:173], off
	v_lshl_add_u64 v[172:173], s[54:55], 0, v[138:139]
	s_add_i32 m0, s76, 0x2000
	s_nop 0
	global_load_lds_dwordx4 v[172:173], off
	s_waitcnt vmcnt(6)
	s_waitcnt lgkmcnt(0)
	s_barrier
	s_setprio 1
	s_waitcnt lgkmcnt(0)
	v_mfma_scale_f32_16x16x128_f8f6f4 v[128:131], v[222:229], v[164:171], v[128:131], v1, v1 op_sel_hi:[0,0,0]
	v_mfma_scale_f32_16x16x128_f8f6f4 v[124:127], v[230:237], v[164:171], v[124:127], v1, v1 op_sel_hi:[0,0,0]
	v_mfma_scale_f32_16x16x128_f8f6f4 v[116:119], v[222:229], v[182:189], v[116:119], v1, v1 op_sel_hi:[0,0,0]
	v_mfma_scale_f32_16x16x128_f8f6f4 v[108:111], v[230:237], v[182:189], v[108:111], v1, v1 op_sel_hi:[0,0,0]
	v_mfma_scale_f32_16x16x128_f8f6f4 v[100:103], v[222:229], v[190:197], v[100:103], v1, v1 op_sel_hi:[0,0,0]
	v_mfma_scale_f32_16x16x128_f8f6f4 v[92:95], v[230:237], v[190:197], v[92:95], v1, v1 op_sel_hi:[0,0,0]
	v_mfma_scale_f32_16x16x128_f8f6f4 v[84:87], v[222:229], v[198:205], v[84:87], v1, v1 op_sel_hi:[0,0,0]
	v_mfma_scale_f32_16x16x128_f8f6f4 v[76:79], v[230:237], v[198:205], v[76:79], v1, v1 op_sel_hi:[0,0,0]
	s_setprio 0
	s_barrier
	s_add_i32 s76, 0, 0x14000
	s_mov_b32 m0, s45
	v_add_u32_e32 v152, s76, v143
	v_add_u32_e32 v160, s76, v144
	v_lshl_add_u64 v[172:173], s[56:57], 0, v[2:3]
	ds_read_b128 v[148:151], v152
	ds_read_b128 v[156:159], v152 offset:2048
	ds_read_b128 v[152:155], v160
	ds_read_b128 v[160:163], v160 offset:2048
	global_load_lds_dwordx4 v[172:173], off
	v_lshl_add_u64 v[174:175], s[56:57], 0, v[134:135]
	s_mov_b32 m0, s51
	s_nop 0
	global_load_lds_dwordx4 v[174:175], off
	s_waitcnt vmcnt(6)
	s_waitcnt lgkmcnt(0)
	s_barrier
	s_setprio 1
	s_waitcnt lgkmcnt(0)
	v_mfma_scale_f32_16x16x128_f8f6f4 v[120:123], v[148:155], v[164:171], v[120:123], v1, v1 op_sel_hi:[0,0,0]
	v_mfma_scale_f32_16x16x128_f8f6f4 v[112:115], v[156:163], v[164:171], v[112:115], v1, v1 op_sel_hi:[0,0,0]
	v_mfma_scale_f32_16x16x128_f8f6f4 v[104:107], v[148:155], v[182:189], v[104:107], v1, v1 op_sel_hi:[0,0,0]
	v_mfma_scale_f32_16x16x128_f8f6f4 v[96:99], v[156:163], v[182:189], v[96:99], v1, v1 op_sel_hi:[0,0,0]
	v_mfma_scale_f32_16x16x128_f8f6f4 v[88:91], v[148:155], v[190:197], v[88:91], v1, v1 op_sel_hi:[0,0,0]
	v_mfma_scale_f32_16x16x128_f8f6f4 v[80:83], v[156:163], v[190:197], v[80:83], v1, v1 op_sel_hi:[0,0,0]
	v_mfma_scale_f32_16x16x128_f8f6f4 v[72:75], v[148:155], v[198:205], v[72:75], v1, v1 op_sel_hi:[0,0,0]
	v_mfma_scale_f32_16x16x128_f8f6f4 v[68:71], v[156:163], v[198:205], v[68:71], v1, v1 op_sel_hi:[0,0,0]
	s_setprio 0
	s_barrier
	s_add_u32 s80, s58, 0x40000
	s_addc_u32 s81, s59, 0
	s_add_i32 s76, s76, s64
	v_lshl_add_u64 v[176:177], s[80:81], 0, v[136:137]
	s_mov_b32 m0, s76
	ds_read_b128 v[164:167], v146 offset:16384
	ds_read_b128 v[182:185], v146 offset:18432
	ds_read_b128 v[168:171], v147 offset:16384
	ds_read_b128 v[186:189], v147 offset:18432
	ds_read_b128 v[190:193], v146 offset:20480
	ds_read_b128 v[198:201], v146 offset:22528
	ds_read_b128 v[194:197], v147 offset:20480
	ds_read_b128 v[202:205], v147 offset:22528
	global_load_lds_dwordx4 v[176:177], off
	v_lshl_add_u64 v[176:177], s[80:81], 0, v[132:133]
	s_add_i32 m0, s76, 0x2000
	s_nop 0
	global_load_lds_dwordx4 v[176:177], off
	s_waitcnt vmcnt(6)
	s_waitcnt lgkmcnt(0)
	s_barrier
	s_setprio 1
	s_waitcnt lgkmcnt(0)
	v_mfma_scale_f32_16x16x128_f8f6f4 v[56:59], v[148:155], v[164:171], v[56:59], v1, v1 op_sel_hi:[0,0,0]
	v_mfma_scale_f32_16x16x128_f8f6f4 v[48:51], v[156:163], v[164:171], v[48:51], v1, v1 op_sel_hi:[0,0,0]
	v_mfma_scale_f32_16x16x128_f8f6f4 v[40:43], v[148:155], v[182:189], v[40:43], v1, v1 op_sel_hi:[0,0,0]
	v_mfma_scale_f32_16x16x128_f8f6f4 v[32:35], v[156:163], v[182:189], v[32:35], v1, v1 op_sel_hi:[0,0,0]
	v_mfma_scale_f32_16x16x128_f8f6f4 v[24:27], v[148:155], v[190:197], v[24:27], v1, v1 op_sel_hi:[0,0,0]
	v_mfma_scale_f32_16x16x128_f8f6f4 v[16:19], v[156:163], v[190:197], v[16:19], v1, v1 op_sel_hi:[0,0,0]
	v_mfma_scale_f32_16x16x128_f8f6f4 v[8:11], v[148:155], v[198:205], v[8:11], v1, v1 op_sel_hi:[0,0,0]
	v_mfma_scale_f32_16x16x128_f8f6f4 v[4:7], v[156:163], v[198:205], v[4:7], v1, v1 op_sel_hi:[0,0,0]
	s_setprio 0
	s_barrier
	s_add_u32 s80, s56, 0x40000
	s_addc_u32 s81, s57, 0
	s_mov_b32 m0, s66
	v_lshl_add_u64 v[176:177], s[80:81], 0, v[2:3]
	global_load_lds_dwordx4 v[176:177], off
	v_lshl_add_u64 v[176:177], s[80:81], 0, v[134:135]
	s_mov_b32 m0, s67
	s_nop 0
	global_load_lds_dwordx4 v[176:177], off
	s_waitcnt vmcnt(6)
	s_waitcnt lgkmcnt(0)
	s_barrier
	s_setprio 1
	s_waitcnt lgkmcnt(0)
	v_mfma_scale_f32_16x16x128_f8f6f4 v[64:67], v[222:229], v[164:171], v[64:67], v1, v1 op_sel_hi:[0,0,0]
	v_mfma_scale_f32_16x16x128_f8f6f4 v[60:63], v[230:237], v[164:171], v[60:63], v1, v1 op_sel_hi:[0,0,0]
	v_mfma_scale_f32_16x16x128_f8f6f4 v[52:55], v[222:229], v[182:189], v[52:55], v1, v1 op_sel_hi:[0,0,0]
	v_mfma_scale_f32_16x16x128_f8f6f4 v[44:47], v[230:237], v[182:189], v[44:47], v1, v1 op_sel_hi:[0,0,0]
	v_mfma_scale_f32_16x16x128_f8f6f4 v[36:39], v[222:229], v[190:197], v[36:39], v1, v1 op_sel_hi:[0,0,0]
	v_mfma_scale_f32_16x16x128_f8f6f4 v[28:31], v[230:237], v[190:197], v[28:31], v1, v1 op_sel_hi:[0,0,0]
	v_mfma_scale_f32_16x16x128_f8f6f4 v[20:23], v[222:229], v[198:205], v[20:23], v1, v1 op_sel_hi:[0,0,0]
	v_mfma_scale_f32_16x16x128_f8f6f4 v[12:15], v[230:237], v[198:205], v[12:15], v1, v1 op_sel_hi:[0,0,0]
	s_setprio 0
	s_barrier
	v_add_u32_e32 v220, s31, v143
	v_add_u32_e32 v221, s31, v144
	ds_read_b128 v[222:225], v220
	ds_read_b128 v[230:233], v220 offset:2048
	ds_read_b128 v[226:229], v221
	ds_read_b128 v[234:237], v221 offset:2048
	s_add_i32 s76, vcc_lo, s64
	v_lshl_add_u64 v[176:177], s[58:59], 0, v[136:137]
	s_mov_b32 m0, s76
	ds_read_b128 v[164:167], v146 offset:32768
	ds_read_b128 v[182:185], v146 offset:34816
	ds_read_b128 v[168:171], v147 offset:32768
	ds_read_b128 v[186:189], v147 offset:34816
	ds_read_b128 v[190:193], v146 offset:36864
	ds_read_b128 v[198:201], v146 offset:38912
	ds_read_b128 v[194:197], v147 offset:36864
	ds_read_b128 v[202:205], v147 offset:38912
	global_load_lds_dwordx4 v[176:177], off
	v_lshl_add_u64 v[176:177], s[58:59], 0, v[132:133]
	s_add_i32 m0, s76, 0x2000
	s_nop 0
	global_load_lds_dwordx4 v[176:177], off
	s_waitcnt vmcnt(6)
	s_waitcnt lgkmcnt(0)
	s_barrier
	s_setprio 1
	s_waitcnt lgkmcnt(0)
	v_mfma_scale_f32_16x16x128_f8f6f4 v[128:131], v[222:229], v[164:171], v[128:131], v1, v1 op_sel_hi:[0,0,0]
	v_mfma_scale_f32_16x16x128_f8f6f4 v[124:127], v[230:237], v[164:171], v[124:127], v1, v1 op_sel_hi:[0,0,0]
	v_mfma_scale_f32_16x16x128_f8f6f4 v[116:119], v[222:229], v[182:189], v[116:119], v1, v1 op_sel_hi:[0,0,0]
	v_mfma_scale_f32_16x16x128_f8f6f4 v[108:111], v[230:237], v[182:189], v[108:111], v1, v1 op_sel_hi:[0,0,0]
	v_mfma_scale_f32_16x16x128_f8f6f4 v[100:103], v[222:229], v[190:197], v[100:103], v1, v1 op_sel_hi:[0,0,0]
	v_mfma_scale_f32_16x16x128_f8f6f4 v[92:95], v[230:237], v[190:197], v[92:95], v1, v1 op_sel_hi:[0,0,0]
	v_mfma_scale_f32_16x16x128_f8f6f4 v[84:87], v[222:229], v[198:205], v[84:87], v1, v1 op_sel_hi:[0,0,0]
	v_mfma_scale_f32_16x16x128_f8f6f4 v[76:79], v[230:237], v[198:205], v[76:79], v1, v1 op_sel_hi:[0,0,0]
	s_setprio 0
	s_barrier
	s_add_i32 s76, 0, 0x1c000
	s_mov_b32 m0, s72
	v_add_u32_e32 v152, s76, v143
	v_add_u32_e32 v160, s76, v144
	v_lshl_add_u64 v[172:173], v[172:173], 0, s[20:21]
	ds_read_b128 v[148:151], v152
	ds_read_b128 v[156:159], v152 offset:2048
	ds_read_b128 v[152:155], v160
	ds_read_b128 v[160:163], v160 offset:2048
	global_load_lds_dwordx4 v[172:173], off
	v_lshl_add_u64 v[172:173], v[174:175], 0, s[20:21]
	s_mov_b32 m0, s73
	s_nop 0
	global_load_lds_dwordx4 v[172:173], off
	s_waitcnt vmcnt(6)
	s_waitcnt lgkmcnt(0)
	s_barrier
	s_setprio 1
	s_waitcnt lgkmcnt(0)
	v_mfma_scale_f32_16x16x128_f8f6f4 v[120:123], v[148:155], v[164:171], v[120:123], v1, v1 op_sel_hi:[0,0,0]
	v_mfma_scale_f32_16x16x128_f8f6f4 v[112:115], v[156:163], v[164:171], v[112:115], v1, v1 op_sel_hi:[0,0,0]
	v_mfma_scale_f32_16x16x128_f8f6f4 v[104:107], v[148:155], v[182:189], v[104:107], v1, v1 op_sel_hi:[0,0,0]
	v_mfma_scale_f32_16x16x128_f8f6f4 v[96:99], v[156:163], v[182:189], v[96:99], v1, v1 op_sel_hi:[0,0,0]
	v_mfma_scale_f32_16x16x128_f8f6f4 v[88:91], v[148:155], v[190:197], v[88:91], v1, v1 op_sel_hi:[0,0,0]
	v_mfma_scale_f32_16x16x128_f8f6f4 v[80:83], v[156:163], v[190:197], v[80:83], v1, v1 op_sel_hi:[0,0,0]
	v_mfma_scale_f32_16x16x128_f8f6f4 v[72:75], v[148:155], v[198:205], v[72:75], v1, v1 op_sel_hi:[0,0,0]
	v_mfma_scale_f32_16x16x128_f8f6f4 v[68:71], v[156:163], v[198:205], v[68:71], v1, v1 op_sel_hi:[0,0,0]
	s_setprio 0
	s_barrier
	s_add_u32 s58, s58, 0x40080
	s_addc_u32 s59, s59, 0
	s_add_i32 s76, s76, s64
	v_lshl_add_u64 v[172:173], s[58:59], 0, v[136:137]
	s_mov_b32 m0, s76
	ds_read_b128 v[164:167], v146 offset:49152
	ds_read_b128 v[182:185], v146 offset:51200
	ds_read_b128 v[168:171], v147 offset:49152
	ds_read_b128 v[186:189], v147 offset:51200
	ds_read_b128 v[190:193], v146 offset:53248
	ds_read_b128 v[198:201], v146 offset:55296
	ds_read_b128 v[194:197], v147 offset:53248
	ds_read_b128 v[202:205], v147 offset:55296
	global_load_lds_dwordx4 v[172:173], off
	v_lshl_add_u64 v[172:173], s[58:59], 0, v[132:133]
	s_add_i32 m0, s76, 0x2000
	s_nop 0
	global_load_lds_dwordx4 v[172:173], off
	s_waitcnt vmcnt(6)
	s_waitcnt lgkmcnt(0)
	s_barrier
	s_setprio 1
	s_waitcnt lgkmcnt(0)
	v_mfma_scale_f32_16x16x128_f8f6f4 v[56:59], v[148:155], v[164:171], v[56:59], v1, v1 op_sel_hi:[0,0,0]
	v_mfma_scale_f32_16x16x128_f8f6f4 v[48:51], v[156:163], v[164:171], v[48:51], v1, v1 op_sel_hi:[0,0,0]
	v_mfma_scale_f32_16x16x128_f8f6f4 v[40:43], v[148:155], v[182:189], v[40:43], v1, v1 op_sel_hi:[0,0,0]
	v_mfma_scale_f32_16x16x128_f8f6f4 v[32:35], v[156:163], v[182:189], v[32:35], v1, v1 op_sel_hi:[0,0,0]
	v_mfma_scale_f32_16x16x128_f8f6f4 v[24:27], v[148:155], v[190:197], v[24:27], v1, v1 op_sel_hi:[0,0,0]
	v_mfma_scale_f32_16x16x128_f8f6f4 v[16:19], v[156:163], v[190:197], v[16:19], v1, v1 op_sel_hi:[0,0,0]
	v_mfma_scale_f32_16x16x128_f8f6f4 v[8:11], v[148:155], v[198:205], v[8:11], v1, v1 op_sel_hi:[0,0,0]
	v_mfma_scale_f32_16x16x128_f8f6f4 v[4:7], v[156:163], v[198:205], v[4:7], v1, v1 op_sel_hi:[0,0,0]
	s_setprio 0
	s_barrier
	s_add_u32 s56, s56, 0x40080
	s_addc_u32 s57, s57, 0
	s_mov_b32 m0, s74
	v_lshl_add_u64 v[172:173], s[56:57], 0, v[2:3]
	global_load_lds_dwordx4 v[172:173], off
	v_lshl_add_u64 v[172:173], s[56:57], 0, v[134:135]
	s_mov_b32 m0, s75
	s_nop 0
	global_load_lds_dwordx4 v[172:173], off
	s_waitcnt vmcnt(6)
	s_waitcnt lgkmcnt(0)
	s_barrier
	s_setprio 1
	s_waitcnt lgkmcnt(0)
	v_mfma_scale_f32_16x16x128_f8f6f4 v[64:67], v[222:229], v[164:171], v[64:67], v1, v1 op_sel_hi:[0,0,0]
	v_mfma_scale_f32_16x16x128_f8f6f4 v[60:63], v[230:237], v[164:171], v[60:63], v1, v1 op_sel_hi:[0,0,0]
	v_mfma_scale_f32_16x16x128_f8f6f4 v[52:55], v[222:229], v[182:189], v[52:55], v1, v1 op_sel_hi:[0,0,0]
	v_mfma_scale_f32_16x16x128_f8f6f4 v[44:47], v[230:237], v[182:189], v[44:47], v1, v1 op_sel_hi:[0,0,0]
	v_mfma_scale_f32_16x16x128_f8f6f4 v[36:39], v[222:229], v[190:197], v[36:39], v1, v1 op_sel_hi:[0,0,0]
	v_mfma_scale_f32_16x16x128_f8f6f4 v[28:31], v[230:237], v[190:197], v[28:31], v1, v1 op_sel_hi:[0,0,0]
	v_mfma_scale_f32_16x16x128_f8f6f4 v[20:23], v[222:229], v[198:205], v[20:23], v1, v1 op_sel_hi:[0,0,0]
	v_mfma_scale_f32_16x16x128_f8f6f4 v[12:15], v[230:237], v[198:205], v[12:15], v1, v1 op_sel_hi:[0,0,0]
	s_setprio 0
	s_barrier
	s_add_i32 s97, s97, 2
	s_add_u32 s89, s89, 0x100
	s_addc_u32 s96, s96, 0
	s_add_u32 s54, s54, 0x100
	s_addc_u32 s55, s55, 0
	s_cmp_gt_u32 s97, 13
	s_cbranch_scc0 .LBB0_430
	v_mul_f32_e32 v152, 0x3c000000, v128
	v_mul_f32_e32 v129, 0x3c000000, v129
	v_mov_b32_e32 v128, v3
	v_cvt_pk_fp8_f32 v128, v152, v129
	v_mul_f32_e32 v124, 0x3c000000, v124
	v_mul_f32_e32 v125, 0x3c000000, v125
	v_mov_b32_e32 v129, v3
	v_cvt_pk_fp8_f32 v129, v124, v125
	v_mul_f32_e32 v124, 0x3c000000, v126
	v_mul_f32_e32 v125, 0x3c000000, v127
	v_mul_f32_e32 v121, 0x3c000000, v121
	v_cvt_pk_fp8_f32 v129, v124, v125 op_sel:[0,0,1]
	v_mul_f32_e32 v124, 0x3c000000, v120
	v_mov_b32_e32 v120, v3
	v_cvt_pk_fp8_f32 v120, v124, v121
	v_mul_f32_e32 v112, 0x3c000000, v112
	v_mul_f32_e32 v113, 0x3c000000, v113
	v_mov_b32_e32 v121, v3
	v_cvt_pk_fp8_f32 v121, v112, v113
	v_mul_f32_e32 v130, 0x3c000000, v130
	v_mul_f32_e32 v131, 0x3c000000, v131
	v_lshl_add_u32 v148, s50, 8, v142
	v_lshl_or_b32 v150, s44, 8, v145
	v_cvt_pk_fp8_f32 v128, v130, v131 op_sel:[0,0,1]
	v_mul_f32_e32 v122, 0x3c000000, v122
	v_mul_f32_e32 v123, 0x3c000000, v123
	v_mul_f32_e32 v112, 0x3c000000, v114
	v_mul_f32_e32 v113, 0x3c000000, v115
	v_ashrrev_i32_e32 v151, 31, v150
	v_ashrrev_i32_e32 v149, 31, v148
	v_cvt_pk_fp8_f32 v120, v122, v123 op_sel:[0,0,1]
	v_cvt_pk_fp8_f32 v121, v112, v113 op_sel:[0,0,1]
	v_lshl_add_u64 v[150:151], s[0:1], 0, v[150:151]
	v_lshlrev_b64 v[112:113], 11, v[148:149]
	v_lshl_add_u64 v[112:113], v[150:151], 0, v[112:113]
	global_store_dwordx2 v[112:113], v[128:129], off
	global_store_dwordx2 v[112:113], v[120:121], off offset:128
	v_mul_f32_e32 v120, 0x3c000000, v116
	v_mul_f32_e32 v117, 0x3c000000, v117
	v_mov_b32_e32 v116, v3
	v_cvt_pk_fp8_f32 v116, v120, v117
	v_mul_f32_e32 v108, 0x3c000000, v108
	v_mul_f32_e32 v109, 0x3c000000, v109
	v_mov_b32_e32 v117, v3
	v_cvt_pk_fp8_f32 v117, v108, v109
	v_mul_f32_e32 v108, 0x3c000000, v110
	v_mul_f32_e32 v109, 0x3c000000, v111
	v_mul_f32_e32 v105, 0x3c000000, v105
	v_cvt_pk_fp8_f32 v117, v108, v109 op_sel:[0,0,1]
	v_mul_f32_e32 v108, 0x3c000000, v104
	v_mov_b32_e32 v104, v3
	v_cvt_pk_fp8_f32 v104, v108, v105
	v_mul_f32_e32 v96, 0x3c000000, v96
	v_mul_f32_e32 v97, 0x3c000000, v97
	v_mov_b32_e32 v105, v3
	v_cvt_pk_fp8_f32 v105, v96, v97
	v_mul_f32_e32 v96, 0x3c000000, v98
	v_mul_f32_e32 v97, 0x3c000000, v99
	v_mul_f32_e32 v99, 0x3c000000, v100
	v_mul_f32_e32 v100, 0x3c000000, v101
	v_mov_b32_e32 v98, v3
	v_cvt_pk_fp8_f32 v98, v99, v100
	v_mul_f32_e32 v92, 0x3c000000, v92
	v_mul_f32_e32 v93, 0x3c000000, v93
	v_mov_b32_e32 v99, v3
	v_cvt_pk_fp8_f32 v99, v92, v93
	v_mul_f32_e32 v92, 0x3c000000, v94
	v_mul_f32_e32 v93, 0x3c000000, v95
	v_mul_f32_e32 v89, 0x3c000000, v89
	v_cvt_pk_fp8_f32 v99, v92, v93 op_sel:[0,0,1]
	v_mul_f32_e32 v92, 0x3c000000, v88
	v_mov_b32_e32 v88, v3
	v_cvt_pk_fp8_f32 v88, v92, v89
	v_mul_f32_e32 v80, 0x3c000000, v80
	v_mul_f32_e32 v81, 0x3c000000, v81
	v_mov_b32_e32 v89, v3
	v_cvt_pk_fp8_f32 v89, v80, v81
	v_mul_f32_e32 v80, 0x3c000000, v82
	v_mul_f32_e32 v81, 0x3c000000, v83
	v_mul_f32_e32 v83, 0x3c000000, v84
	v_mul_f32_e32 v84, 0x3c000000, v85
	v_mov_b32_e32 v82, v3
	v_cvt_pk_fp8_f32 v82, v83, v84
	v_mul_f32_e32 v76, 0x3c000000, v76
	v_mul_f32_e32 v77, 0x3c000000, v77
	v_mov_b32_e32 v83, v3
	v_cvt_pk_fp8_f32 v83, v76, v77
	v_mul_f32_e32 v76, 0x3c000000, v78
	v_mul_f32_e32 v77, 0x3c000000, v79
	v_mul_f32_e32 v73, 0x3c000000, v73
	v_cvt_pk_fp8_f32 v83, v76, v77 op_sel:[0,0,1]
	v_mul_f32_e32 v76, 0x3c000000, v72
	v_mov_b32_e32 v72, v3
	v_cvt_pk_fp8_f32 v72, v76, v73
	v_mul_f32_e32 v68, 0x3c000000, v68
	v_mul_f32_e32 v69, 0x3c000000, v69
	v_mov_b32_e32 v73, v3
	v_cvt_pk_fp8_f32 v73, v68, v69
	v_mul_f32_e32 v68, 0x3c000000, v70
	v_mul_f32_e32 v70, 0x3c000000, v64
	v_mul_f32_e32 v65, 0x3c000000, v65
	v_mov_b32_e32 v64, v3
	v_cvt_pk_fp8_f32 v64, v70, v65
	v_mul_f32_e32 v60, 0x3c000000, v60
	v_mul_f32_e32 v61, 0x3c000000, v61
	v_mov_b32_e32 v65, v3
	v_cvt_pk_fp8_f32 v65, v60, v61
	v_mul_f32_e32 v60, 0x3c000000, v62
	v_mul_f32_e32 v61, 0x3c000000, v63
	v_mul_f32_e32 v57, 0x3c000000, v57
	v_cvt_pk_fp8_f32 v65, v60, v61 op_sel:[0,0,1]
	v_mul_f32_e32 v60, 0x3c000000, v56
	v_mov_b32_e32 v56, v3
	v_cvt_pk_fp8_f32 v56, v60, v57
	v_mul_f32_e32 v48, 0x3c000000, v48
	v_mul_f32_e32 v49, 0x3c000000, v49
	v_mov_b32_e32 v57, v3
	v_cvt_pk_fp8_f32 v57, v48, v49
	v_mul_f32_e32 v48, 0x3c000000, v50
	v_mul_f32_e32 v49, 0x3c000000, v51
	v_mul_f32_e32 v51, 0x3c000000, v52
	v_mul_f32_e32 v52, 0x3c000000, v53
	v_mov_b32_e32 v50, v3
	v_cvt_pk_fp8_f32 v50, v51, v52
	v_mul_f32_e32 v44, 0x3c000000, v44
	v_mul_f32_e32 v45, 0x3c000000, v45
	v_mov_b32_e32 v51, v3
	v_cvt_pk_fp8_f32 v51, v44, v45
	v_mul_f32_e32 v44, 0x3c000000, v46
	v_mul_f32_e32 v45, 0x3c000000, v47
	v_mul_f32_e32 v41, 0x3c000000, v41
	v_cvt_pk_fp8_f32 v51, v44, v45 op_sel:[0,0,1]
	v_mul_f32_e32 v44, 0x3c000000, v40
	v_mov_b32_e32 v40, v3
	v_cvt_pk_fp8_f32 v40, v44, v41
	v_mul_f32_e32 v32, 0x3c000000, v32
	v_mul_f32_e32 v33, 0x3c000000, v33
	v_mov_b32_e32 v41, v3
	v_cvt_pk_fp8_f32 v41, v32, v33
	v_mul_f32_e32 v32, 0x3c000000, v34
	v_mul_f32_e32 v33, 0x3c000000, v35
	v_mul_f32_e32 v35, 0x3c000000, v36
	v_mul_f32_e32 v36, 0x3c000000, v37
	v_mov_b32_e32 v34, v3
	v_cvt_pk_fp8_f32 v34, v35, v36
	v_mul_f32_e32 v28, 0x3c000000, v28
	v_mul_f32_e32 v29, 0x3c000000, v29
	v_mov_b32_e32 v35, v3
	v_cvt_pk_fp8_f32 v35, v28, v29
	v_mul_f32_e32 v28, 0x3c000000, v30
	v_mul_f32_e32 v29, 0x3c000000, v31
	v_mul_f32_e32 v25, 0x3c000000, v25
	v_cvt_pk_fp8_f32 v35, v28, v29 op_sel:[0,0,1]
	v_mul_f32_e32 v28, 0x3c000000, v24
	v_mov_b32_e32 v24, v3
	v_mul_f32_e32 v118, 0x3c000000, v118
	v_mul_f32_e32 v119, 0x3c000000, v119
	v_cvt_pk_fp8_f32 v24, v28, v25
	v_mul_f32_e32 v16, 0x3c000000, v16
	v_mul_f32_e32 v17, 0x3c000000, v17
	v_mov_b32_e32 v25, v3
	v_or_b32_e32 v114, 16, v148
	v_cvt_pk_fp8_f32 v116, v118, v119 op_sel:[0,0,1]
	v_mul_f32_e32 v106, 0x3c000000, v106
	v_mul_f32_e32 v107, 0x3c000000, v107
	v_cvt_pk_fp8_f32 v25, v16, v17
	v_mul_f32_e32 v16, 0x3c000000, v18
	v_mul_f32_e32 v17, 0x3c000000, v19
	v_mul_f32_e32 v19, 0x3c000000, v20
	v_mul_f32_e32 v20, 0x3c000000, v21
	v_mov_b32_e32 v18, v3
	v_ashrrev_i32_e32 v115, 31, v114
	v_cvt_pk_fp8_f32 v104, v106, v107 op_sel:[0,0,1]
	v_cvt_pk_fp8_f32 v105, v96, v97 op_sel:[0,0,1]
	v_cvt_pk_fp8_f32 v18, v19, v20
	v_mul_f32_e32 v12, 0x3c000000, v12
	v_mul_f32_e32 v13, 0x3c000000, v13
	v_mov_b32_e32 v19, v3
	v_lshlrev_b64 v[96:97], 11, v[114:115]
	v_cvt_pk_fp8_f32 v19, v12, v13
	v_lshl_add_u64 v[96:97], v[150:151], 0, v[96:97]
	v_mul_f32_e32 v100, 0x3c000000, v102
	v_mul_f32_e32 v101, 0x3c000000, v103
	global_store_dwordx2 v[96:97], v[116:117], off
	global_store_dwordx2 v[96:97], v[104:105], off offset:128
	v_or_b32_e32 v96, 32, v148
	v_cvt_pk_fp8_f32 v98, v100, v101 op_sel:[0,0,1]
	v_mul_f32_e32 v90, 0x3c000000, v90
	v_mul_f32_e32 v91, 0x3c000000, v91
	v_ashrrev_i32_e32 v97, 31, v96
	v_cvt_pk_fp8_f32 v88, v90, v91 op_sel:[0,0,1]
	v_cvt_pk_fp8_f32 v89, v80, v81 op_sel:[0,0,1]
	s_mov_b32 s5, 0x40000
	v_mul_f32_e32 v12, 0x3c000000, v14
	v_mul_f32_e32 v13, 0x3c000000, v15
	v_lshlrev_b64 v[80:81], 11, v[96:97]
	v_cvt_pk_fp8_f32 v57, v48, v49 op_sel:[0,0,1]
	v_add_co_u32_e32 v48, vcc, s5, v112
	v_cvt_pk_fp8_f32 v19, v12, v13 op_sel:[0,0,1]
	v_mul_f32_e32 v12, 0x3c000000, v8
	v_mul_f32_e32 v9, 0x3c000000, v9
	v_mov_b32_e32 v8, v3
	v_lshl_add_u64 v[80:81], v[150:151], 0, v[80:81]
	v_mul_f32_e32 v84, 0x3c000000, v86
	v_mul_f32_e32 v85, 0x3c000000, v87
	v_addc_co_u32_e32 v49, vcc, 0, v113, vcc
	s_mov_b32 s5, 0x48000
	v_cvt_pk_fp8_f32 v8, v12, v9
	v_mul_f32_e32 v4, 0x3c000000, v4
	v_mul_f32_e32 v5, 0x3c000000, v5
	v_mov_b32_e32 v9, v3
	global_store_dwordx2 v[80:81], v[98:99], off
	global_store_dwordx2 v[80:81], v[88:89], off offset:128
	v_or_b32_e32 v80, 48, v148
	v_cvt_pk_fp8_f32 v82, v84, v85 op_sel:[0,0,1]
	v_mul_f32_e32 v74, 0x3c000000, v74
	v_mul_f32_e32 v75, 0x3c000000, v75
	v_mul_f32_e32 v69, 0x3c000000, v71
	v_mul_f32_e32 v66, 0x3c000000, v66
	v_mul_f32_e32 v67, 0x3c000000, v67
	v_cvt_pk_fp8_f32 v41, v32, v33 op_sel:[0,0,1]
	v_add_co_u32_e32 v32, vcc, s5, v112
	v_cvt_pk_fp8_f32 v9, v4, v5
	v_ashrrev_i32_e32 v81, 31, v80
	v_cvt_pk_fp8_f32 v72, v74, v75 op_sel:[0,0,1]
	v_cvt_pk_fp8_f32 v73, v68, v69 op_sel:[0,0,1]
	v_cvt_pk_fp8_f32 v64, v66, v67 op_sel:[0,0,1]
	v_mul_f32_e32 v58, 0x3c000000, v58
	v_mul_f32_e32 v59, 0x3c000000, v59
	v_mul_f32_e32 v52, 0x3c000000, v54
	v_mul_f32_e32 v53, 0x3c000000, v55
	v_addc_co_u32_e32 v33, vcc, 0, v113, vcc
	s_mov_b32 s5, 0x50000
	v_lshlrev_b64 v[68:69], 11, v[80:81]
	v_cvt_pk_fp8_f32 v56, v58, v59 op_sel:[0,0,1]
	v_cvt_pk_fp8_f32 v50, v52, v53 op_sel:[0,0,1]
	v_mul_f32_e32 v42, 0x3c000000, v42
	v_mul_f32_e32 v43, 0x3c000000, v43
	v_mul_f32_e32 v36, 0x3c000000, v38
	v_mul_f32_e32 v37, 0x3c000000, v39
	v_cvt_pk_fp8_f32 v25, v16, v17 op_sel:[0,0,1]
	v_add_co_u32_e32 v16, vcc, s5, v112
	v_mul_f32_e32 v20, 0x3c000000, v22
	v_mul_f32_e32 v21, 0x3c000000, v23
	v_lshl_add_u64 v[68:69], v[150:151], 0, v[68:69]
	s_mov_b64 s[8:9], 0x40000
	v_cvt_pk_fp8_f32 v40, v42, v43 op_sel:[0,0,1]
	v_cvt_pk_fp8_f32 v34, v36, v37 op_sel:[0,0,1]
	v_mul_f32_e32 v26, 0x3c000000, v26
	v_mul_f32_e32 v27, 0x3c000000, v27
	v_addc_co_u32_e32 v17, vcc, 0, v113, vcc
	v_cvt_pk_fp8_f32 v18, v20, v21 op_sel:[0,0,1]
	v_mul_f32_e32 v10, 0x3c000000, v10
	v_mul_f32_e32 v11, 0x3c000000, v11
	v_mul_f32_e32 v4, 0x3c000000, v6
	v_mul_f32_e32 v5, 0x3c000000, v7
	s_mov_b32 s5, 0x58000
	global_store_dwordx2 v[68:69], v[82:83], off
	global_store_dwordx2 v[68:69], v[72:73], off offset:128
	v_lshl_add_u64 v[68:69], v[112:113], 0, s[8:9]
	s_mov_b64 s[8:9], 0x48000
	v_cvt_pk_fp8_f32 v24, v26, v27 op_sel:[0,0,1]
	v_cvt_pk_fp8_f32 v8, v10, v11 op_sel:[0,0,1]
	v_cvt_pk_fp8_f32 v9, v4, v5 op_sel:[0,0,1]
	v_add_co_u32_e32 v4, vcc, s5, v112
	global_store_dwordx2 v[48:49], v[64:65], off
	global_store_dwordx2 v[68:69], v[56:57], off offset:128
	v_lshl_add_u64 v[48:49], v[112:113], 0, s[8:9]
	s_mov_b64 s[8:9], 0x50000
	v_addc_co_u32_e32 v5, vcc, 0, v113, vcc
	global_store_dwordx2 v[32:33], v[50:51], off
	global_store_dwordx2 v[48:49], v[40:41], off offset:128
	v_lshl_add_u64 v[32:33], v[112:113], 0, s[8:9]
	s_mov_b64 s[8:9], 0x58000
	s_and_b64 vcc, exec, s[40:41]
	s_mov_b32 s44, s4
	s_mov_b32 s50, s42
	s_mov_b64 s[54:55], s[52:53]
	s_mov_b64 s[56:57], s[46:47]
	global_store_dwordx2 v[16:17], v[34:35], off
	global_store_dwordx2 v[32:33], v[24:25], off offset:128
	v_lshl_add_u64 v[16:17], v[112:113], 0, s[8:9]
	global_store_dwordx2 v[4:5], v[18:19], off
	global_store_dwordx2 v[16:17], v[8:9], off offset:128
	s_cbranch_vccz .LBB0_427
	s_waitcnt vmcnt(0)
	v_readlane_b32 s86, v253, 23
	v_readlane_b32 s88, v253, 25
	s_cmpk_gt_u32 s27, 0xff
	v_readlane_b32 s84, v253, 20
	v_readlane_b32 s76, v253, 22
	v_readlane_b32 s87, v253, 24
	v_readlane_b32 s89, v253, 26
	v_readlane_b32 s85, v253, 21
	s_cbranch_scc1 .LBB0_434
	s_barrier

.LBB0_605:
	s_add_u32 s56, s54, 0x80
	s_addc_u32 s57, s55, 0
	s_add_i32 vcc_lo, 0, 0x10000
	v_add_u32_e32 v220, vcc_lo, v145
	v_add_u32_e32 v221, vcc_lo, v146
	ds_read_b128 v[222:225], v220
	ds_read_b128 v[230:233], v220 offset:2048
	ds_read_b128 v[226:229], v221
	ds_read_b128 v[234:237], v221 offset:2048
	s_cmp_eq_u32 s97, 12
	s_cselect_b32 s59, s45, s57
	s_cselect_b32 s58, s47, s56
	s_cselect_b32 s57, s8, s96
	s_cselect_b32 s56, s9, s89
	s_add_i32 s76, s31, s64
	v_lshl_add_u64 v[142:143], s[54:55], 0, v[140:141]
	s_mov_b32 m0, s76
	ds_read_b128 v[166:169], v148
	ds_read_b128 v[182:185], v148 offset:2048
	ds_read_b128 v[170:173], v149
	ds_read_b128 v[186:189], v149 offset:2048
	ds_read_b128 v[190:193], v148 offset:4096
	ds_read_b128 v[198:201], v148 offset:6144
	ds_read_b128 v[194:197], v149 offset:4096
	ds_read_b128 v[202:205], v149 offset:6144
	global_load_lds_dwordx4 v[142:143], off
	v_lshl_add_u64 v[142:143], s[54:55], 0, v[138:139]
	s_add_i32 m0, s76, 0x2000
	s_nop 0
	global_load_lds_dwordx4 v[142:143], off
	s_waitcnt vmcnt(6)
	s_waitcnt lgkmcnt(0)
	s_barrier
	s_setprio 1
	s_waitcnt lgkmcnt(0)
	v_mfma_scale_f32_16x16x128_f8f6f4 v[128:131], v[222:229], v[166:173], v[128:131], v1, v1 op_sel_hi:[0,0,0]
	v_mfma_scale_f32_16x16x128_f8f6f4 v[124:127], v[230:237], v[166:173], v[124:127], v1, v1 op_sel_hi:[0,0,0]
	v_mfma_scale_f32_16x16x128_f8f6f4 v[120:123], v[222:229], v[182:189], v[120:123], v1, v1 op_sel_hi:[0,0,0]
	v_mfma_scale_f32_16x16x128_f8f6f4 v[112:115], v[230:237], v[182:189], v[112:115], v1, v1 op_sel_hi:[0,0,0]
	v_mfma_scale_f32_16x16x128_f8f6f4 v[104:107], v[222:229], v[190:197], v[104:107], v1, v1 op_sel_hi:[0,0,0]
	v_mfma_scale_f32_16x16x128_f8f6f4 v[96:99], v[230:237], v[190:197], v[96:99], v1, v1 op_sel_hi:[0,0,0]
	v_mfma_scale_f32_16x16x128_f8f6f4 v[88:91], v[222:229], v[198:205], v[88:91], v1, v1 op_sel_hi:[0,0,0]
	v_mfma_scale_f32_16x16x128_f8f6f4 v[80:83], v[230:237], v[198:205], v[80:83], v1, v1 op_sel_hi:[0,0,0]
	s_setprio 0
	s_barrier
	s_add_i32 s76, 0, 0x14000
	v_add_u32_e32 v142, s76, v145
	v_add_u32_e32 v143, s76, v146
	s_mov_b32 m0, s5
	ds_read_b128 v[150:153], v142
	ds_read_b128 v[158:161], v142 offset:2048
	ds_read_b128 v[154:157], v143
	ds_read_b128 v[162:165], v143 offset:2048
	v_lshl_add_u64 v[142:143], s[56:57], 0, v[2:3]
	global_load_lds_dwordx4 v[142:143], off
	v_lshl_add_u64 v[174:175], s[56:57], 0, v[134:135]
	s_mov_b32 m0, s43
	s_nop 0
	global_load_lds_dwordx4 v[174:175], off
	s_waitcnt vmcnt(6)
	s_waitcnt lgkmcnt(0)
	s_barrier
	s_setprio 1
	s_waitcnt lgkmcnt(0)
	v_mfma_scale_f32_16x16x128_f8f6f4 v[116:119], v[150:157], v[166:173], v[116:119], v1, v1 op_sel_hi:[0,0,0]
	v_mfma_scale_f32_16x16x128_f8f6f4 v[108:111], v[158:165], v[166:173], v[108:111], v1, v1 op_sel_hi:[0,0,0]
	v_mfma_scale_f32_16x16x128_f8f6f4 v[100:103], v[150:157], v[182:189], v[100:103], v1, v1 op_sel_hi:[0,0,0]
	v_mfma_scale_f32_16x16x128_f8f6f4 v[92:95], v[158:165], v[182:189], v[92:95], v1, v1 op_sel_hi:[0,0,0]
	v_mfma_scale_f32_16x16x128_f8f6f4 v[84:87], v[150:157], v[190:197], v[84:87], v1, v1 op_sel_hi:[0,0,0]
	v_mfma_scale_f32_16x16x128_f8f6f4 v[76:79], v[158:165], v[190:197], v[76:79], v1, v1 op_sel_hi:[0,0,0]
	v_mfma_scale_f32_16x16x128_f8f6f4 v[72:75], v[150:157], v[198:205], v[72:75], v1, v1 op_sel_hi:[0,0,0]
	v_mfma_scale_f32_16x16x128_f8f6f4 v[68:71], v[158:165], v[198:205], v[68:71], v1, v1 op_sel_hi:[0,0,0]
	s_setprio 0
	s_barrier
	s_add_u32 s80, s58, 0x40000
	s_addc_u32 s81, s59, 0
	s_add_i32 s76, s76, s64
	v_lshl_add_u64 v[176:177], s[80:81], 0, v[136:137]
	s_mov_b32 m0, s76
	ds_read_b128 v[166:169], v148 offset:16384
	ds_read_b128 v[182:185], v148 offset:18432
	ds_read_b128 v[170:173], v149 offset:16384
	ds_read_b128 v[186:189], v149 offset:18432
	ds_read_b128 v[190:193], v148 offset:20480
	ds_read_b128 v[198:201], v148 offset:22528
	ds_read_b128 v[194:197], v149 offset:20480
	ds_read_b128 v[202:205], v149 offset:22528
	global_load_lds_dwordx4 v[176:177], off
	v_lshl_add_u64 v[176:177], s[80:81], 0, v[132:133]
	s_add_i32 m0, s76, 0x2000
	s_nop 0
	global_load_lds_dwordx4 v[176:177], off
	s_waitcnt vmcnt(6)
	s_waitcnt lgkmcnt(0)
	s_barrier
	s_setprio 1
	s_waitcnt lgkmcnt(0)
	v_mfma_scale_f32_16x16x128_f8f6f4 v[52:55], v[150:157], v[166:173], v[52:55], v1, v1 op_sel_hi:[0,0,0]
	v_mfma_scale_f32_16x16x128_f8f6f4 v[44:47], v[158:165], v[166:173], v[44:47], v1, v1 op_sel_hi:[0,0,0]
	v_mfma_scale_f32_16x16x128_f8f6f4 v[36:39], v[150:157], v[182:189], v[36:39], v1, v1 op_sel_hi:[0,0,0]
	v_mfma_scale_f32_16x16x128_f8f6f4 v[28:31], v[158:165], v[182:189], v[28:31], v1, v1 op_sel_hi:[0,0,0]
	v_mfma_scale_f32_16x16x128_f8f6f4 v[20:23], v[150:157], v[190:197], v[20:23], v1, v1 op_sel_hi:[0,0,0]
	v_mfma_scale_f32_16x16x128_f8f6f4 v[12:15], v[158:165], v[190:197], v[12:15], v1, v1 op_sel_hi:[0,0,0]
	v_mfma_scale_f32_16x16x128_f8f6f4 v[8:11], v[150:157], v[198:205], v[8:11], v1, v1 op_sel_hi:[0,0,0]
	v_mfma_scale_f32_16x16x128_f8f6f4 v[4:7], v[158:165], v[198:205], v[4:7], v1, v1 op_sel_hi:[0,0,0]
	s_setprio 0
	s_barrier
	s_add_u32 s80, s56, 0x40000
	s_addc_u32 s81, s57, 0
	s_mov_b32 m0, s66
	v_lshl_add_u64 v[176:177], s[80:81], 0, v[2:3]
	global_load_lds_dwordx4 v[176:177], off
	v_lshl_add_u64 v[176:177], s[80:81], 0, v[134:135]
	s_mov_b32 m0, s67
	s_nop 0
	global_load_lds_dwordx4 v[176:177], off
	s_waitcnt vmcnt(6)
	s_waitcnt lgkmcnt(0)
	s_barrier
	s_setprio 1
	s_waitcnt lgkmcnt(0)
	v_mfma_scale_f32_16x16x128_f8f6f4 v[64:67], v[222:229], v[166:173], v[64:67], v1, v1 op_sel_hi:[0,0,0]
	v_mfma_scale_f32_16x16x128_f8f6f4 v[60:63], v[230:237], v[166:173], v[60:63], v1, v1 op_sel_hi:[0,0,0]
	v_mfma_scale_f32_16x16x128_f8f6f4 v[56:59], v[222:229], v[182:189], v[56:59], v1, v1 op_sel_hi:[0,0,0]
	v_mfma_scale_f32_16x16x128_f8f6f4 v[48:51], v[230:237], v[182:189], v[48:51], v1, v1 op_sel_hi:[0,0,0]
	v_mfma_scale_f32_16x16x128_f8f6f4 v[40:43], v[222:229], v[190:197], v[40:43], v1, v1 op_sel_hi:[0,0,0]
	v_mfma_scale_f32_16x16x128_f8f6f4 v[32:35], v[230:237], v[190:197], v[32:35], v1, v1 op_sel_hi:[0,0,0]
	v_mfma_scale_f32_16x16x128_f8f6f4 v[24:27], v[222:229], v[198:205], v[24:27], v1, v1 op_sel_hi:[0,0,0]
	v_mfma_scale_f32_16x16x128_f8f6f4 v[16:19], v[230:237], v[198:205], v[16:19], v1, v1 op_sel_hi:[0,0,0]
	s_setprio 0
	s_barrier
	v_add_u32_e32 v220, s31, v145
	v_add_u32_e32 v221, s31, v146
	ds_read_b128 v[222:225], v220
	ds_read_b128 v[230:233], v220 offset:2048
	ds_read_b128 v[226:229], v221
	ds_read_b128 v[234:237], v221 offset:2048
	s_add_i32 s76, vcc_lo, s64
	v_lshl_add_u64 v[176:177], s[58:59], 0, v[136:137]
	s_mov_b32 m0, s76
	ds_read_b128 v[166:169], v148 offset:32768
	ds_read_b128 v[182:185], v148 offset:34816
	ds_read_b128 v[170:173], v149 offset:32768
	ds_read_b128 v[186:189], v149 offset:34816
	ds_read_b128 v[190:193], v148 offset:36864
	ds_read_b128 v[198:201], v148 offset:38912
	ds_read_b128 v[194:197], v149 offset:36864
	ds_read_b128 v[202:205], v149 offset:38912
	global_load_lds_dwordx4 v[176:177], off
	v_lshl_add_u64 v[176:177], s[58:59], 0, v[132:133]
	s_add_i32 m0, s76, 0x2000
	s_nop 0
	global_load_lds_dwordx4 v[176:177], off
	s_waitcnt vmcnt(6)
	s_waitcnt lgkmcnt(0)
	s_barrier
	s_setprio 1
	s_waitcnt lgkmcnt(0)
	v_mfma_scale_f32_16x16x128_f8f6f4 v[128:131], v[222:229], v[166:173], v[128:131], v1, v1 op_sel_hi:[0,0,0]
	v_mfma_scale_f32_16x16x128_f8f6f4 v[124:127], v[230:237], v[166:173], v[124:127], v1, v1 op_sel_hi:[0,0,0]
	v_mfma_scale_f32_16x16x128_f8f6f4 v[120:123], v[222:229], v[182:189], v[120:123], v1, v1 op_sel_hi:[0,0,0]
	v_mfma_scale_f32_16x16x128_f8f6f4 v[112:115], v[230:237], v[182:189], v[112:115], v1, v1 op_sel_hi:[0,0,0]
	v_mfma_scale_f32_16x16x128_f8f6f4 v[104:107], v[222:229], v[190:197], v[104:107], v1, v1 op_sel_hi:[0,0,0]
	v_mfma_scale_f32_16x16x128_f8f6f4 v[96:99], v[230:237], v[190:197], v[96:99], v1, v1 op_sel_hi:[0,0,0]
	v_mfma_scale_f32_16x16x128_f8f6f4 v[88:91], v[222:229], v[198:205], v[88:91], v1, v1 op_sel_hi:[0,0,0]
	v_mfma_scale_f32_16x16x128_f8f6f4 v[80:83], v[230:237], v[198:205], v[80:83], v1, v1 op_sel_hi:[0,0,0]
	s_setprio 0
	s_barrier
	s_add_i32 s76, 0, 0x1c000
	s_mov_b32 m0, s72
	v_add_u32_e32 v154, s76, v145
	v_add_u32_e32 v162, s76, v146
	v_lshl_add_u64 v[142:143], v[142:143], 0, s[20:21]
	ds_read_b128 v[150:153], v154
	ds_read_b128 v[158:161], v154 offset:2048
	ds_read_b128 v[154:157], v162
	ds_read_b128 v[162:165], v162 offset:2048
	global_load_lds_dwordx4 v[142:143], off
	v_lshl_add_u64 v[142:143], v[174:175], 0, s[20:21]
	s_mov_b32 m0, s73
	s_nop 0
	global_load_lds_dwordx4 v[142:143], off
	s_waitcnt vmcnt(6)
	s_waitcnt lgkmcnt(0)
	s_barrier
	s_setprio 1
	s_waitcnt lgkmcnt(0)
	v_mfma_scale_f32_16x16x128_f8f6f4 v[116:119], v[150:157], v[166:173], v[116:119], v1, v1 op_sel_hi:[0,0,0]
	v_mfma_scale_f32_16x16x128_f8f6f4 v[108:111], v[158:165], v[166:173], v[108:111], v1, v1 op_sel_hi:[0,0,0]
	v_mfma_scale_f32_16x16x128_f8f6f4 v[100:103], v[150:157], v[182:189], v[100:103], v1, v1 op_sel_hi:[0,0,0]
	v_mfma_scale_f32_16x16x128_f8f6f4 v[92:95], v[158:165], v[182:189], v[92:95], v1, v1 op_sel_hi:[0,0,0]
	v_mfma_scale_f32_16x16x128_f8f6f4 v[84:87], v[150:157], v[190:197], v[84:87], v1, v1 op_sel_hi:[0,0,0]
	v_mfma_scale_f32_16x16x128_f8f6f4 v[76:79], v[158:165], v[190:197], v[76:79], v1, v1 op_sel_hi:[0,0,0]
	v_mfma_scale_f32_16x16x128_f8f6f4 v[72:75], v[150:157], v[198:205], v[72:75], v1, v1 op_sel_hi:[0,0,0]
	v_mfma_scale_f32_16x16x128_f8f6f4 v[68:71], v[158:165], v[198:205], v[68:71], v1, v1 op_sel_hi:[0,0,0]
	s_setprio 0
	s_barrier
	s_add_u32 s58, s58, 0x40080
	s_addc_u32 s59, s59, 0
	s_add_i32 s76, s76, s64
	v_lshl_add_u64 v[142:143], s[58:59], 0, v[136:137]
	s_mov_b32 m0, s76
	ds_read_b128 v[166:169], v148 offset:49152
	ds_read_b128 v[182:185], v148 offset:51200
	ds_read_b128 v[170:173], v149 offset:49152
	ds_read_b128 v[186:189], v149 offset:51200
	ds_read_b128 v[190:193], v148 offset:53248
	ds_read_b128 v[198:201], v148 offset:55296
	ds_read_b128 v[194:197], v149 offset:53248
	ds_read_b128 v[202:205], v149 offset:55296
	global_load_lds_dwordx4 v[142:143], off
	v_lshl_add_u64 v[142:143], s[58:59], 0, v[132:133]
	s_add_i32 m0, s76, 0x2000
	s_nop 0
	global_load_lds_dwordx4 v[142:143], off
	s_waitcnt vmcnt(6)
	s_waitcnt lgkmcnt(0)
	s_barrier
	s_setprio 1
	s_waitcnt lgkmcnt(0)
	v_mfma_scale_f32_16x16x128_f8f6f4 v[52:55], v[150:157], v[166:173], v[52:55], v1, v1 op_sel_hi:[0,0,0]
	v_mfma_scale_f32_16x16x128_f8f6f4 v[44:47], v[158:165], v[166:173], v[44:47], v1, v1 op_sel_hi:[0,0,0]
	v_mfma_scale_f32_16x16x128_f8f6f4 v[36:39], v[150:157], v[182:189], v[36:39], v1, v1 op_sel_hi:[0,0,0]
	v_mfma_scale_f32_16x16x128_f8f6f4 v[28:31], v[158:165], v[182:189], v[28:31], v1, v1 op_sel_hi:[0,0,0]
	v_mfma_scale_f32_16x16x128_f8f6f4 v[20:23], v[150:157], v[190:197], v[20:23], v1, v1 op_sel_hi:[0,0,0]
	v_mfma_scale_f32_16x16x128_f8f6f4 v[12:15], v[158:165], v[190:197], v[12:15], v1, v1 op_sel_hi:[0,0,0]
	v_mfma_scale_f32_16x16x128_f8f6f4 v[8:11], v[150:157], v[198:205], v[8:11], v1, v1 op_sel_hi:[0,0,0]
	v_mfma_scale_f32_16x16x128_f8f6f4 v[4:7], v[158:165], v[198:205], v[4:7], v1, v1 op_sel_hi:[0,0,0]
	s_setprio 0
	s_barrier
	s_add_u32 s56, s56, 0x40080
	s_addc_u32 s57, s57, 0
	s_mov_b32 m0, s74
	v_lshl_add_u64 v[142:143], s[56:57], 0, v[2:3]
	global_load_lds_dwordx4 v[142:143], off
	v_lshl_add_u64 v[142:143], s[56:57], 0, v[134:135]
	s_mov_b32 m0, s75
	s_nop 0
	global_load_lds_dwordx4 v[142:143], off
	s_waitcnt vmcnt(6)
	s_waitcnt lgkmcnt(0)
	s_barrier
	s_setprio 1
	s_waitcnt lgkmcnt(0)
	v_mfma_scale_f32_16x16x128_f8f6f4 v[64:67], v[222:229], v[166:173], v[64:67], v1, v1 op_sel_hi:[0,0,0]
	v_mfma_scale_f32_16x16x128_f8f6f4 v[60:63], v[230:237], v[166:173], v[60:63], v1, v1 op_sel_hi:[0,0,0]
	v_mfma_scale_f32_16x16x128_f8f6f4 v[56:59], v[222:229], v[182:189], v[56:59], v1, v1 op_sel_hi:[0,0,0]
	v_mfma_scale_f32_16x16x128_f8f6f4 v[48:51], v[230:237], v[182:189], v[48:51], v1, v1 op_sel_hi:[0,0,0]
	v_mfma_scale_f32_16x16x128_f8f6f4 v[40:43], v[222:229], v[190:197], v[40:43], v1, v1 op_sel_hi:[0,0,0]
	v_mfma_scale_f32_16x16x128_f8f6f4 v[32:35], v[230:237], v[190:197], v[32:35], v1, v1 op_sel_hi:[0,0,0]
	v_mfma_scale_f32_16x16x128_f8f6f4 v[24:27], v[222:229], v[198:205], v[24:27], v1, v1 op_sel_hi:[0,0,0]
	v_mfma_scale_f32_16x16x128_f8f6f4 v[16:19], v[230:237], v[198:205], v[16:19], v1, v1 op_sel_hi:[0,0,0]
	s_setprio 0
	s_barrier
	s_add_i32 s97, s97, 2
	s_add_u32 s89, s89, 0x100
	s_addc_u32 s96, s96, 0
	s_add_u32 s54, s54, 0x100
	s_addc_u32 s55, s55, 0
	s_cmp_gt_u32 s97, 13
	s_cbranch_scc0 .LBB0_605
	v_lshl_add_u32 v150, s42, 8, v144
	v_lshl_or_b32 v142, s4, 8, v147
	v_ashrrev_i32_e32 v151, 31, v150
	v_ashrrev_i32_e32 v143, 31, v142
	v_lshlrev_b64 v[152:153], 12, v[150:151]
	v_lshl_add_u64 v[152:153], s[0:1], 0, v[152:153]
	v_lshlrev_b64 v[154:155], 1, v[142:143]
	v_lshl_add_u64 v[142:143], v[152:153], 0, v[154:155]
	v_pk_mul_f32 v[130:131], v[130:131], s[22:23] op_sel_hi:[1,0]
	v_pk_mul_f32 v[128:129], v[128:129], s[22:23] op_sel_hi:[1,0]
	v_pk_mul_f32 v[152:153], v[126:127], s[22:23] op_sel_hi:[1,0]
	v_pk_mul_f32 v[126:127], v[124:125], s[22:23] op_sel_hi:[1,0]
	v_cvt_pk_bf16_f32 v124, v128, v129
	v_cvt_pk_bf16_f32 v125, v130, v131
	v_cvt_pk_bf16_f32 v126, v126, v127
	v_cvt_pk_bf16_f32 v127, v152, v153
	global_store_dwordx4 v[142:143], v[124:127], off
	v_pk_mul_f32 v[118:119], v[118:119], s[22:23] op_sel_hi:[1,0]
	v_pk_mul_f32 v[116:117], v[116:117], s[22:23] op_sel_hi:[1,0]
	v_pk_mul_f32 v[124:125], v[110:111], s[22:23] op_sel_hi:[1,0]
	v_pk_mul_f32 v[110:111], v[108:109], s[22:23] op_sel_hi:[1,0]
	v_cvt_pk_bf16_f32 v108, v116, v117
	v_cvt_pk_bf16_f32 v109, v118, v119
	v_cvt_pk_bf16_f32 v110, v110, v111
	v_cvt_pk_bf16_f32 v111, v124, v125
	global_store_dwordx4 v[142:143], v[108:111], off offset:256
	v_pk_mul_f32 v[114:115], v[114:115], s[22:23] op_sel_hi:[1,0]
	v_pk_mul_f32 v[112:113], v[112:113], s[22:23] op_sel_hi:[1,0]
	v_or_b32_e32 v108, 16, v150
	v_ashrrev_i32_e32 v109, 31, v108
	v_lshlrev_b64 v[108:109], 12, v[108:109]
	v_lshl_add_u64 v[108:109], s[0:1], 0, v[108:109]
	v_lshl_add_u64 v[116:117], v[108:109], 0, v[154:155]
	v_pk_mul_f32 v[110:111], v[122:123], s[22:23] op_sel_hi:[1,0]
	v_pk_mul_f32 v[108:109], v[120:121], s[22:23] op_sel_hi:[1,0]
	v_pk_mul_f32 v[102:103], v[102:103], s[22:23] op_sel_hi:[1,0]
	v_cvt_pk_bf16_f32 v108, v108, v109
	v_cvt_pk_bf16_f32 v109, v110, v111
	v_cvt_pk_bf16_f32 v110, v112, v113
	v_cvt_pk_bf16_f32 v111, v114, v115
	global_store_dwordx4 v[116:117], v[108:111], off
	v_pk_mul_f32 v[100:101], v[100:101], s[22:23] op_sel_hi:[1,0]
	v_pk_mul_f32 v[98:99], v[98:99], s[22:23] op_sel_hi:[1,0]
	v_pk_mul_f32 v[108:109], v[94:95], s[22:23] op_sel_hi:[1,0]
	v_pk_mul_f32 v[94:95], v[92:93], s[22:23] op_sel_hi:[1,0]
	v_cvt_pk_bf16_f32 v92, v100, v101
	v_cvt_pk_bf16_f32 v93, v102, v103
	v_cvt_pk_bf16_f32 v94, v94, v95
	v_cvt_pk_bf16_f32 v95, v108, v109
	global_store_dwordx4 v[116:117], v[92:95], off offset:256
	v_pk_mul_f32 v[96:97], v[96:97], s[22:23] op_sel_hi:[1,0]
	v_pk_mul_f32 v[86:87], v[86:87], s[22:23] op_sel_hi:[1,0]
	v_or_b32_e32 v92, 32, v150
	v_ashrrev_i32_e32 v93, 31, v92
	v_lshlrev_b64 v[92:93], 12, v[92:93]
	v_lshl_add_u64 v[92:93], s[0:1], 0, v[92:93]
	v_lshl_add_u64 v[100:101], v[92:93], 0, v[154:155]
	v_pk_mul_f32 v[94:95], v[106:107], s[22:23] op_sel_hi:[1,0]
	v_pk_mul_f32 v[92:93], v[104:105], s[22:23] op_sel_hi:[1,0]
	v_pk_mul_f32 v[84:85], v[84:85], s[22:23] op_sel_hi:[1,0]
	v_cvt_pk_bf16_f32 v92, v92, v93
	v_cvt_pk_bf16_f32 v93, v94, v95
	v_cvt_pk_bf16_f32 v94, v96, v97
	v_cvt_pk_bf16_f32 v95, v98, v99
	global_store_dwordx4 v[100:101], v[92:95], off
	v_pk_mul_f32 v[82:83], v[82:83], s[22:23] op_sel_hi:[1,0]
	v_pk_mul_f32 v[80:81], v[80:81], s[22:23] op_sel_hi:[1,0]
	v_pk_mul_f32 v[92:93], v[78:79], s[22:23] op_sel_hi:[1,0]
	v_pk_mul_f32 v[78:79], v[76:77], s[22:23] op_sel_hi:[1,0]
	v_cvt_pk_bf16_f32 v76, v84, v85
	v_cvt_pk_bf16_f32 v77, v86, v87
	v_cvt_pk_bf16_f32 v78, v78, v79
	v_cvt_pk_bf16_f32 v79, v92, v93
	global_store_dwordx4 v[100:101], v[76:79], off offset:256
	v_pk_mul_f32 v[74:75], v[74:75], s[22:23] op_sel_hi:[1,0]
	v_pk_mul_f32 v[72:73], v[72:73], s[22:23] op_sel_hi:[1,0]
	v_or_b32_e32 v76, 48, v150
	v_ashrrev_i32_e32 v77, 31, v76
	v_lshlrev_b64 v[76:77], 12, v[76:77]
	v_lshl_add_u64 v[76:77], s[0:1], 0, v[76:77]
	v_lshl_add_u64 v[84:85], v[76:77], 0, v[154:155]
	v_pk_mul_f32 v[78:79], v[90:91], s[22:23] op_sel_hi:[1,0]
	v_pk_mul_f32 v[76:77], v[88:89], s[22:23] op_sel_hi:[1,0]
	v_pk_mul_f32 v[64:65], v[64:65], s[22:23] op_sel_hi:[1,0]
	v_cvt_pk_bf16_f32 v76, v76, v77
	v_cvt_pk_bf16_f32 v77, v78, v79
	v_cvt_pk_bf16_f32 v78, v80, v81
	v_cvt_pk_bf16_f32 v79, v82, v83
	global_store_dwordx4 v[84:85], v[76:79], off
	s_mov_b32 s4, 0x80000
	v_pk_mul_f32 v[66:67], v[66:67], s[22:23] op_sel_hi:[1,0]
	v_pk_mul_f32 v[76:77], v[70:71], s[22:23] op_sel_hi:[1,0]
	v_pk_mul_f32 v[70:71], v[68:69], s[22:23] op_sel_hi:[1,0]
	v_cvt_pk_bf16_f32 v68, v72, v73
	v_cvt_pk_bf16_f32 v69, v74, v75
	v_cvt_pk_bf16_f32 v70, v70, v71
	v_cvt_pk_bf16_f32 v71, v76, v77
	global_store_dwordx4 v[84:85], v[68:71], off offset:256
	s_mov_b64 s[8:9], 0x80000
	v_pk_mul_f32 v[54:55], v[54:55], s[22:23] op_sel_hi:[1,0]
	v_pk_mul_f32 v[70:71], v[62:63], s[22:23] op_sel_hi:[1,0]
	v_pk_mul_f32 v[62:63], v[60:61], s[22:23] op_sel_hi:[1,0]
	v_cvt_pk_bf16_f32 v60, v64, v65
	v_add_co_u32_e32 v64, vcc, s4, v142
	v_cvt_pk_bf16_f32 v61, v66, v67
	v_cvt_pk_bf16_f32 v62, v62, v63
	v_cvt_pk_bf16_f32 v63, v70, v71
	v_addc_co_u32_e32 v65, vcc, 0, v143, vcc
	global_store_dwordx4 v[64:65], v[60:63], off
	v_pk_mul_f32 v[52:53], v[52:53], s[22:23] op_sel_hi:[1,0]
	v_lshl_add_u64 v[68:69], v[142:143], 0, s[8:9]
	v_pk_mul_f32 v[60:61], v[46:47], s[22:23] op_sel_hi:[1,0]
	v_pk_mul_f32 v[46:47], v[44:45], s[22:23] op_sel_hi:[1,0]
	v_cvt_pk_bf16_f32 v44, v52, v53
	v_cvt_pk_bf16_f32 v45, v54, v55
	v_cvt_pk_bf16_f32 v46, v46, v47
	v_cvt_pk_bf16_f32 v47, v60, v61
	global_store_dwordx4 v[68:69], v[44:47], off offset:256
	v_pk_mul_f32 v[48:49], v[48:49], s[22:23] op_sel_hi:[1,0]
	s_mov_b32 s4, 0x90000
	v_pk_mul_f32 v[46:47], v[58:59], s[22:23] op_sel_hi:[1,0]
	v_pk_mul_f32 v[44:45], v[56:57], s[22:23] op_sel_hi:[1,0]
	v_pk_mul_f32 v[50:51], v[50:51], s[22:23] op_sel_hi:[1,0]
	v_cvt_pk_bf16_f32 v44, v44, v45
	v_cvt_pk_bf16_f32 v45, v46, v47
	v_cvt_pk_bf16_f32 v46, v48, v49
	v_add_co_u32_e32 v48, vcc, s4, v142
	v_cvt_pk_bf16_f32 v47, v50, v51
	s_nop 0
	v_addc_co_u32_e32 v49, vcc, 0, v143, vcc
	s_mov_b64 s[8:9], 0x90000
	global_store_dwordx4 v[48:49], v[44:47], off
	v_pk_mul_f32 v[38:39], v[38:39], s[22:23] op_sel_hi:[1,0]
	v_pk_mul_f32 v[36:37], v[36:37], s[22:23] op_sel_hi:[1,0]
	v_pk_mul_f32 v[44:45], v[30:31], s[22:23] op_sel_hi:[1,0]
	v_pk_mul_f32 v[30:31], v[28:29], s[22:23] op_sel_hi:[1,0]
	v_lshl_add_u64 v[52:53], v[142:143], 0, s[8:9]
	v_cvt_pk_bf16_f32 v28, v36, v37
	v_cvt_pk_bf16_f32 v29, v38, v39
	v_cvt_pk_bf16_f32 v30, v30, v31
	v_cvt_pk_bf16_f32 v31, v44, v45
	global_store_dwordx4 v[52:53], v[28:31], off offset:256
	v_pk_mul_f32 v[32:33], v[32:33], s[22:23] op_sel_hi:[1,0]
	s_mov_b32 s4, 0xa0000
	v_pk_mul_f32 v[30:31], v[42:43], s[22:23] op_sel_hi:[1,0]
	v_pk_mul_f32 v[28:29], v[40:41], s[22:23] op_sel_hi:[1,0]
	v_pk_mul_f32 v[34:35], v[34:35], s[22:23] op_sel_hi:[1,0]
	v_cvt_pk_bf16_f32 v28, v28, v29
	v_cvt_pk_bf16_f32 v29, v30, v31
	v_cvt_pk_bf16_f32 v30, v32, v33
	v_add_co_u32_e32 v32, vcc, s4, v142
	v_cvt_pk_bf16_f32 v31, v34, v35
	s_nop 0
	v_addc_co_u32_e32 v33, vcc, 0, v143, vcc
	s_mov_b64 s[8:9], 0xa0000
	global_store_dwordx4 v[32:33], v[28:31], off
	v_pk_mul_f32 v[22:23], v[22:23], s[22:23] op_sel_hi:[1,0]
	v_pk_mul_f32 v[20:21], v[20:21], s[22:23] op_sel_hi:[1,0]
	v_pk_mul_f32 v[28:29], v[14:15], s[22:23] op_sel_hi:[1,0]
	v_pk_mul_f32 v[14:15], v[12:13], s[22:23] op_sel_hi:[1,0]
	v_lshl_add_u64 v[36:37], v[142:143], 0, s[8:9]
	v_cvt_pk_bf16_f32 v12, v20, v21
	v_cvt_pk_bf16_f32 v13, v22, v23
	v_cvt_pk_bf16_f32 v14, v14, v15
	v_cvt_pk_bf16_f32 v15, v28, v29
	global_store_dwordx4 v[36:37], v[12:15], off offset:256
	v_pk_mul_f32 v[16:17], v[16:17], s[22:23] op_sel_hi:[1,0]
	s_mov_b32 s4, 0xb0000
	v_pk_mul_f32 v[14:15], v[26:27], s[22:23] op_sel_hi:[1,0]
	v_pk_mul_f32 v[12:13], v[24:25], s[22:23] op_sel_hi:[1,0]
	v_pk_mul_f32 v[18:19], v[18:19], s[22:23] op_sel_hi:[1,0]
	v_cvt_pk_bf16_f32 v12, v12, v13
	v_cvt_pk_bf16_f32 v13, v14, v15
	v_cvt_pk_bf16_f32 v14, v16, v17
	v_add_co_u32_e32 v16, vcc, s4, v142
	v_cvt_pk_bf16_f32 v15, v18, v19
	s_nop 0
	v_addc_co_u32_e32 v17, vcc, 0, v143, vcc
	s_mov_b64 s[8:9], 0xb0000
	global_store_dwordx4 v[16:17], v[12:15], off
	v_pk_mul_f32 v[10:11], v[10:11], s[22:23] op_sel_hi:[1,0]
	v_pk_mul_f32 v[8:9], v[8:9], s[22:23] op_sel_hi:[1,0]
	v_pk_mul_f32 v[12:13], v[6:7], s[22:23] op_sel_hi:[1,0]
	v_pk_mul_f32 v[6:7], v[4:5], s[22:23] op_sel_hi:[1,0]
	v_lshl_add_u64 v[20:21], v[142:143], 0, s[8:9]
	v_cvt_pk_bf16_f32 v4, v8, v9
	v_cvt_pk_bf16_f32 v5, v10, v11
	v_cvt_pk_bf16_f32 v6, v6, v7
	v_cvt_pk_bf16_f32 v7, v12, v13
	s_and_b64 vcc, exec, s[40:41]
	s_mov_b32 s4, s44
	s_mov_b32 s42, s46
	s_mov_b64 s[54:55], s[52:53]
	s_mov_b64 s[56:57], s[50:51]
	global_store_dwordx4 v[20:21], v[4:7], off offset:256
	s_cbranch_vccz .LBB0_602
	s_waitcnt vmcnt(0)
	v_readlane_b32 s86, v253, 23
	v_readlane_b32 s88, v253, 25
	s_cmpk_gt_u32 s27, 0xff
	v_readlane_b32 s84, v253, 20
	v_readlane_b32 s76, v253, 22
	v_readlane_b32 s87, v253, 24
	v_readlane_b32 s89, v253, 26
	v_readlane_b32 s85, v253, 21
	s_cbranch_scc1 .LBB0_609
	s_barrier
